# speedup vs baseline: 1.0203x; 1.0150x over previous
.LBB6_12:
	ds_read_b128 v[176:179], v169
	ds_read_b128 v[180:183], v170
	ds_read_b128 v[184:187], v171
	ds_read_b128 v[188:191], v172
	v_add_u32_e32 v174, 0xc000, v152
	v_lshl_add_u64 v[192:193], v[136:137], 0, s[44:45]
	v_readfirstlane_b32 s47, v174
	v_add_u32_e32 v175, 0xe000, v152
	v_add_u32_e32 v173, s17, v168
	v_lshl_add_u64 v[232:233], v[192:193], 0, s[30:31]
	s_mov_b32 m0, s47
	v_lshl_add_u64 v[248:249], v[134:135], 0, s[44:45]
	v_readfirstlane_b32 s47, v175
	ds_read_b128 v[196:199], v173
	ds_read_b128 v[200:203], v173 offset:1024
	ds_read_b128 v[204:207], v173 offset:2048
	ds_read_b128 v[212:215], v173 offset:3072
	ds_read_b128 v[216:219], v173 offset:4096
	ds_read_b128 v[220:223], v173 offset:5120
	ds_read_b128 v[224:227], v173 offset:6144
	ds_read_b128 v[228:231], v173 offset:7168
	global_load_lds_dwordx4 v[232:233], off
	v_lshl_add_u64 v[232:233], v[248:249], 0, s[30:31]
	s_mov_b32 m0, s47
	s_nop 0
	global_load_lds_dwordx4 v[232:233], off
	s_waitcnt lgkmcnt(8)
	s_barrier
	s_waitcnt lgkmcnt(0)
	s_waitcnt lgkmcnt(0)
	v_mfma_f32_16x16x32_f16 v[2:5], v[196:199], v[176:179], v[2:5]
	v_mfma_f32_16x16x32_f16 v[6:9], v[196:199], v[184:187], v[6:9]
	v_mfma_f32_16x16x32_f16 v[10:13], v[204:207], v[176:179], v[10:13]
	v_mfma_f32_16x16x32_f16 v[18:21], v[204:207], v[184:187], v[18:21]
	v_mfma_f32_16x16x32_f16 v[30:33], v[216:219], v[176:179], v[30:33]
	v_mfma_f32_16x16x32_f16 v[42:45], v[216:219], v[184:187], v[42:45]
	v_mfma_f32_16x16x32_f16 v[54:57], v[224:227], v[176:179], v[54:57]
	v_mfma_f32_16x16x32_f16 v[66:69], v[224:227], v[184:187], v[66:69]
	v_mfma_f32_16x16x32_f16 v[2:5], v[200:203], v[180:183], v[2:5]
	v_mfma_f32_16x16x32_f16 v[6:9], v[200:203], v[188:191], v[6:9]
	v_mfma_f32_16x16x32_f16 v[10:13], v[212:215], v[180:183], v[10:13]
	v_mfma_f32_16x16x32_f16 v[18:21], v[212:215], v[188:191], v[18:21]
	v_mfma_f32_16x16x32_f16 v[30:33], v[220:223], v[180:183], v[30:33]
	v_mfma_f32_16x16x32_f16 v[42:45], v[220:223], v[188:191], v[42:45]
	v_mfma_f32_16x16x32_f16 v[54:57], v[228:231], v[180:183], v[54:57]
	v_mfma_f32_16x16x32_f16 v[66:69], v[228:231], v[188:191], v[66:69]
	s_barrier
	v_lshl_add_u64 v[250:251], v[140:141], 0, s[44:45]
	v_readfirstlane_b32 s47, v146
	v_lshl_add_u64 v[252:253], v[250:251], 0, s[34:35]
	s_mov_b32 m0, s47
	ds_read_b128 v[232:235], v161
	ds_read_b128 v[236:239], v162
	ds_read_b128 v[240:243], v163
	ds_read_b128 v[244:247], v164
	global_load_lds_dwordx4 v[252:253], off
	v_lshl_add_u64 v[252:253], v[138:139], 0, s[44:45]
	v_readfirstlane_b32 s47, v147
	v_lshl_add_u64 v[254:255], v[252:253], 0, s[34:35]
	s_mov_b32 m0, s47
	s_nop 0
	global_load_lds_dwordx4 v[254:255], off
	s_barrier
	s_waitcnt lgkmcnt(0)
	s_waitcnt lgkmcnt(0)
	v_mfma_f32_16x16x32_f16 v[14:17], v[196:199], v[232:235], v[14:17]
	v_mfma_f32_16x16x32_f16 v[22:25], v[196:199], v[240:243], v[22:25]
	v_mfma_f32_16x16x32_f16 v[34:37], v[204:207], v[232:235], v[34:37]
	v_mfma_f32_16x16x32_f16 v[46:49], v[204:207], v[240:243], v[46:49]
	v_mfma_f32_16x16x32_f16 v[58:61], v[216:219], v[232:235], v[58:61]
	v_mfma_f32_16x16x32_f16 v[70:73], v[216:219], v[240:243], v[70:73]
	v_mfma_f32_16x16x32_f16 v[78:81], v[224:227], v[232:235], v[78:81]
	v_mfma_f32_16x16x32_f16 v[86:89], v[224:227], v[240:243], v[86:89]
	v_mfma_f32_16x16x32_f16 v[14:17], v[200:203], v[236:239], v[14:17]
	v_mfma_f32_16x16x32_f16 v[22:25], v[200:203], v[244:247], v[22:25]
	v_mfma_f32_16x16x32_f16 v[34:37], v[212:215], v[236:239], v[34:37]
	v_mfma_f32_16x16x32_f16 v[46:49], v[212:215], v[244:247], v[46:49]
	v_mfma_f32_16x16x32_f16 v[58:61], v[220:223], v[236:239], v[58:61]
	v_mfma_f32_16x16x32_f16 v[70:73], v[220:223], v[244:247], v[70:73]
	v_mfma_f32_16x16x32_f16 v[78:81], v[228:231], v[236:239], v[78:81]
	v_mfma_f32_16x16x32_f16 v[86:89], v[228:231], v[244:247], v[86:89]
	v_readfirstlane_b32 s47, v152
	v_lshl_add_u64 v[254:255], v[192:193], 0, s[34:35]
	s_mov_b32 m0, s47
	v_readfirstlane_b32 s47, v153
	s_barrier
	ds_read_b128 v[196:199], v173 offset:16384
	ds_read_b128 v[200:203], v173 offset:17408
	ds_read_b128 v[204:207], v173 offset:18432
	ds_read_b128 v[212:215], v173 offset:19456
	ds_read_b128 v[216:219], v173 offset:20480
	ds_read_b128 v[220:223], v173 offset:21504
	ds_read_b128 v[224:227], v173 offset:22528
	ds_read_b128 v[228:231], v173 offset:23552
	global_load_lds_dwordx4 v[254:255], off
	v_lshl_add_u64 v[254:255], v[248:249], 0, s[34:35]
	s_mov_b32 m0, s47
	s_nop 0
	global_load_lds_dwordx4 v[254:255], off
	s_barrier
	s_waitcnt lgkmcnt(0)
	s_waitcnt lgkmcnt(0)
	v_mfma_f32_16x16x32_f16 v[26:29], v[196:199], v[176:179], v[26:29]
	v_mfma_f32_16x16x32_f16 v[38:41], v[196:199], v[184:187], v[38:41]
	v_mfma_f32_16x16x32_f16 v[50:53], v[204:207], v[176:179], v[50:53]
	v_mfma_f32_16x16x32_f16 v[62:65], v[204:207], v[184:187], v[62:65]
	v_mfma_f32_16x16x32_f16 v[74:77], v[216:219], v[176:179], v[74:77]
	v_mfma_f32_16x16x32_f16 v[82:85], v[216:219], v[184:187], v[82:85]
	v_mfma_f32_16x16x32_f16 v[90:93], v[224:227], v[176:179], v[90:93]
	v_mfma_f32_16x16x32_f16 v[94:97], v[224:227], v[184:187], v[94:97]
	v_mfma_f32_16x16x32_f16 v[26:29], v[200:203], v[180:183], v[26:29]
	v_mfma_f32_16x16x32_f16 v[38:41], v[200:203], v[188:191], v[38:41]
	v_mfma_f32_16x16x32_f16 v[50:53], v[212:215], v[180:183], v[50:53]
	v_mfma_f32_16x16x32_f16 v[62:65], v[212:215], v[188:191], v[62:65]
	v_mfma_f32_16x16x32_f16 v[74:77], v[220:223], v[180:183], v[74:77]
	v_mfma_f32_16x16x32_f16 v[82:85], v[220:223], v[188:191], v[82:85]
	v_mfma_f32_16x16x32_f16 v[90:93], v[228:231], v[180:183], v[90:93]
	v_mfma_f32_16x16x32_f16 v[94:97], v[228:231], v[188:191], v[94:97]
	s_barrier
	v_readfirstlane_b32 s47, v154
	v_lshl_add_u64 v[176:177], v[250:251], 0, s[36:37]
	s_mov_b32 m0, s47
	v_readfirstlane_b32 s47, v155
	global_load_lds_dwordx4 v[176:177], off
	v_lshl_add_u64 v[176:177], v[252:253], 0, s[36:37]
	s_mov_b32 m0, s47
	s_nop 0
	global_load_lds_dwordx4 v[176:177], off
	s_waitcnt vmcnt(6)
	s_barrier
	v_mfma_f32_16x16x32_f16 v[98:101], v[196:199], v[232:235], v[98:101]
	v_mfma_f32_16x16x32_f16 v[102:105], v[196:199], v[240:243], v[102:105]
	v_mfma_f32_16x16x32_f16 v[106:109], v[204:207], v[232:235], v[106:109]
	v_mfma_f32_16x16x32_f16 v[110:113], v[204:207], v[240:243], v[110:113]
	v_mfma_f32_16x16x32_f16 v[114:117], v[216:219], v[232:235], v[114:117]
	v_mfma_f32_16x16x32_f16 v[118:121], v[216:219], v[240:243], v[118:121]
	v_mfma_f32_16x16x32_f16 v[122:125], v[224:227], v[232:235], v[122:125]
	v_mfma_f32_16x16x32_f16 v[126:129], v[224:227], v[240:243], v[126:129]
	v_mfma_f32_16x16x32_f16 v[98:101], v[200:203], v[236:239], v[98:101]
	v_mfma_f32_16x16x32_f16 v[102:105], v[200:203], v[244:247], v[102:105]
	v_mfma_f32_16x16x32_f16 v[106:109], v[212:215], v[236:239], v[106:109]
	v_mfma_f32_16x16x32_f16 v[110:113], v[212:215], v[244:247], v[110:113]
	v_mfma_f32_16x16x32_f16 v[114:117], v[220:223], v[236:239], v[114:117]
	v_mfma_f32_16x16x32_f16 v[118:121], v[220:223], v[244:247], v[118:121]
	v_mfma_f32_16x16x32_f16 v[122:125], v[228:231], v[236:239], v[122:125]
	v_mfma_f32_16x16x32_f16 v[126:129], v[228:231], v[244:247], v[126:129]
	s_barrier
	ds_read_b128 v[176:179], v148
	ds_read_b128 v[180:183], v149
	ds_read_b128 v[184:187], v150
	ds_read_b128 v[188:191], v151
	v_readfirstlane_b32 s47, v156
	v_lshl_add_u64 v[232:233], v[192:193], 0, s[36:37]
	s_mov_b32 m0, s47
	v_readfirstlane_b32 s47, v157
	ds_read_b128 v[196:199], v173 offset:32768
	ds_read_b128 v[200:203], v173 offset:33792
	ds_read_b128 v[204:207], v173 offset:34816
	ds_read_b128 v[212:215], v173 offset:35840
	ds_read_b128 v[216:219], v173 offset:36864
	ds_read_b128 v[220:223], v173 offset:37888
	ds_read_b128 v[224:227], v173 offset:38912
	ds_read_b128 v[228:231], v173 offset:39936
	global_load_lds_dwordx4 v[232:233], off
	v_lshl_add_u64 v[232:233], v[248:249], 0, s[36:37]
	s_mov_b32 m0, s47
	s_nop 0
	global_load_lds_dwordx4 v[232:233], off
	s_waitcnt lgkmcnt(8)
	s_barrier
	s_waitcnt lgkmcnt(0)
	s_waitcnt lgkmcnt(0)
	v_mfma_f32_16x16x32_f16 v[2:5], v[196:199], v[176:179], v[2:5]
	v_mfma_f32_16x16x32_f16 v[6:9], v[196:199], v[184:187], v[6:9]
	v_mfma_f32_16x16x32_f16 v[10:13], v[204:207], v[176:179], v[10:13]
	v_mfma_f32_16x16x32_f16 v[18:21], v[204:207], v[184:187], v[18:21]
	v_mfma_f32_16x16x32_f16 v[30:33], v[216:219], v[176:179], v[30:33]
	v_mfma_f32_16x16x32_f16 v[42:45], v[216:219], v[184:187], v[42:45]
	v_mfma_f32_16x16x32_f16 v[54:57], v[224:227], v[176:179], v[54:57]
	v_mfma_f32_16x16x32_f16 v[66:69], v[224:227], v[184:187], v[66:69]
	v_mfma_f32_16x16x32_f16 v[2:5], v[200:203], v[180:183], v[2:5]
	v_mfma_f32_16x16x32_f16 v[6:9], v[200:203], v[188:191], v[6:9]
	v_mfma_f32_16x16x32_f16 v[10:13], v[212:215], v[180:183], v[10:13]
	v_mfma_f32_16x16x32_f16 v[18:21], v[212:215], v[188:191], v[18:21]
	v_mfma_f32_16x16x32_f16 v[30:33], v[220:223], v[180:183], v[30:33]
	v_mfma_f32_16x16x32_f16 v[42:45], v[220:223], v[188:191], v[42:45]
	v_mfma_f32_16x16x32_f16 v[54:57], v[228:231], v[180:183], v[54:57]
	v_mfma_f32_16x16x32_f16 v[66:69], v[228:231], v[188:191], v[66:69]
	s_barrier
	v_readfirstlane_b32 s47, v158
	v_lshl_add_u64 v[254:255], v[250:251], 0, s[38:39]
	s_mov_b32 m0, s47
	v_readfirstlane_b32 s47, v159
	ds_read_b128 v[232:235], v142
	ds_read_b128 v[236:239], v143
	ds_read_b128 v[240:243], v144
	ds_read_b128 v[244:247], v145
	global_load_lds_dwordx4 v[254:255], off
	v_lshl_add_u64 v[254:255], v[252:253], 0, s[38:39]
	s_mov_b32 m0, s47
	s_nop 0
	global_load_lds_dwordx4 v[254:255], off
	s_barrier
	s_waitcnt lgkmcnt(0)
	s_waitcnt lgkmcnt(0)
	v_mfma_f32_16x16x32_f16 v[14:17], v[196:199], v[232:235], v[14:17]
	v_mfma_f32_16x16x32_f16 v[22:25], v[196:199], v[240:243], v[22:25]
	v_mfma_f32_16x16x32_f16 v[34:37], v[204:207], v[232:235], v[34:37]
	v_mfma_f32_16x16x32_f16 v[46:49], v[204:207], v[240:243], v[46:49]
	v_mfma_f32_16x16x32_f16 v[58:61], v[216:219], v[232:235], v[58:61]
	v_mfma_f32_16x16x32_f16 v[70:73], v[216:219], v[240:243], v[70:73]
	v_mfma_f32_16x16x32_f16 v[78:81], v[224:227], v[232:235], v[78:81]
	v_mfma_f32_16x16x32_f16 v[86:89], v[224:227], v[240:243], v[86:89]
	v_mfma_f32_16x16x32_f16 v[14:17], v[200:203], v[236:239], v[14:17]
	v_mfma_f32_16x16x32_f16 v[22:25], v[200:203], v[244:247], v[22:25]
	v_mfma_f32_16x16x32_f16 v[34:37], v[212:215], v[236:239], v[34:37]
	v_mfma_f32_16x16x32_f16 v[46:49], v[212:215], v[244:247], v[46:49]
	v_mfma_f32_16x16x32_f16 v[58:61], v[220:223], v[236:239], v[58:61]
	v_mfma_f32_16x16x32_f16 v[70:73], v[220:223], v[244:247], v[70:73]
	v_mfma_f32_16x16x32_f16 v[78:81], v[228:231], v[236:239], v[78:81]
	v_mfma_f32_16x16x32_f16 v[86:89], v[228:231], v[244:247], v[86:89]
	v_readfirstlane_b32 s47, v160
	v_lshl_add_u64 v[192:193], v[192:193], 0, s[38:39]
	s_mov_b32 m0, s47
	v_readfirstlane_b32 s47, v165
	s_barrier
	ds_read_b128 v[196:199], v173 offset:49152
	ds_read_b128 v[200:203], v173 offset:50176
	ds_read_b128 v[204:207], v173 offset:51200
	ds_read_b128 v[212:215], v173 offset:52224
	ds_read_b128 v[216:219], v173 offset:53248
	ds_read_b128 v[220:223], v173 offset:54272
	ds_read_b128 v[224:227], v173 offset:55296
	ds_read_b128 v[228:231], v173 offset:56320
	global_load_lds_dwordx4 v[192:193], off
	v_lshl_add_u64 v[192:193], v[248:249], 0, s[38:39]
	s_mov_b32 m0, s47
	s_nop 0
	global_load_lds_dwordx4 v[192:193], off
	s_barrier
	s_waitcnt lgkmcnt(0)
	s_waitcnt lgkmcnt(0)
	v_mfma_f32_16x16x32_f16 v[26:29], v[196:199], v[176:179], v[26:29]
	v_mfma_f32_16x16x32_f16 v[38:41], v[196:199], v[184:187], v[38:41]
	v_mfma_f32_16x16x32_f16 v[50:53], v[204:207], v[176:179], v[50:53]
	v_mfma_f32_16x16x32_f16 v[62:65], v[204:207], v[184:187], v[62:65]
	v_mfma_f32_16x16x32_f16 v[74:77], v[216:219], v[176:179], v[74:77]
	v_mfma_f32_16x16x32_f16 v[82:85], v[216:219], v[184:187], v[82:85]
	v_mfma_f32_16x16x32_f16 v[90:93], v[224:227], v[176:179], v[90:93]
	v_mfma_f32_16x16x32_f16 v[94:97], v[224:227], v[184:187], v[94:97]
	v_mfma_f32_16x16x32_f16 v[26:29], v[200:203], v[180:183], v[26:29]
	v_mfma_f32_16x16x32_f16 v[38:41], v[200:203], v[188:191], v[38:41]
	v_mfma_f32_16x16x32_f16 v[50:53], v[212:215], v[180:183], v[50:53]
	v_mfma_f32_16x16x32_f16 v[62:65], v[212:215], v[188:191], v[62:65]
	v_mfma_f32_16x16x32_f16 v[74:77], v[220:223], v[180:183], v[74:77]
	v_mfma_f32_16x16x32_f16 v[82:85], v[220:223], v[188:191], v[82:85]
	v_mfma_f32_16x16x32_f16 v[90:93], v[228:231], v[180:183], v[90:93]
	v_mfma_f32_16x16x32_f16 v[94:97], v[228:231], v[188:191], v[94:97]
	s_barrier
	v_readfirstlane_b32 s47, v166
	v_lshl_add_u64 v[176:177], v[250:251], 0, s[40:41]
	s_mov_b32 m0, s47
	v_readfirstlane_b32 s47, v167
	global_load_lds_dwordx4 v[176:177], off
	v_lshl_add_u64 v[176:177], v[252:253], 0, s[40:41]
	s_mov_b32 m0, s47
	s_nop 0
	global_load_lds_dwordx4 v[176:177], off
	s_waitcnt vmcnt(6)
	s_barrier
	v_mfma_f32_16x16x32_f16 v[98:101], v[196:199], v[232:235], v[98:101]
	v_mfma_f32_16x16x32_f16 v[102:105], v[196:199], v[240:243], v[102:105]
	v_mfma_f32_16x16x32_f16 v[106:109], v[204:207], v[232:235], v[106:109]
	v_mfma_f32_16x16x32_f16 v[110:113], v[204:207], v[240:243], v[110:113]
	v_mfma_f32_16x16x32_f16 v[114:117], v[216:219], v[232:235], v[114:117]
	v_mfma_f32_16x16x32_f16 v[118:121], v[216:219], v[240:243], v[118:121]
	v_mfma_f32_16x16x32_f16 v[122:125], v[224:227], v[232:235], v[122:125]
	v_mfma_f32_16x16x32_f16 v[126:129], v[224:227], v[240:243], v[126:129]
	v_mfma_f32_16x16x32_f16 v[98:101], v[200:203], v[236:239], v[98:101]
	v_mfma_f32_16x16x32_f16 v[102:105], v[200:203], v[244:247], v[102:105]
	v_mfma_f32_16x16x32_f16 v[106:109], v[212:215], v[236:239], v[106:109]
	v_mfma_f32_16x16x32_f16 v[110:113], v[212:215], v[244:247], v[110:113]
	v_mfma_f32_16x16x32_f16 v[114:117], v[220:223], v[236:239], v[114:117]
	v_mfma_f32_16x16x32_f16 v[118:121], v[220:223], v[244:247], v[118:121]
	v_mfma_f32_16x16x32_f16 v[122:125], v[228:231], v[236:239], v[122:125]
	v_mfma_f32_16x16x32_f16 v[126:129], v[228:231], v[244:247], v[126:129]
	s_add_i32 s46, s46, 2
	s_add_u32 s44, s44, 0x100
	s_addc_u32 s45, s45, 0
	s_cmp_lt_u32 s46, 4
	s_barrier
	s_cbranch_scc1 .LBB6_12
	s_add_u32 s0, s0, 0x20380
	s_addc_u32 s1, s1, 0
	v_readfirstlane_b32 s17, v174
	v_lshl_add_u64 v[130:131], v[130:131], 1, s[0:1]
	s_mov_b32 m0, s17
	ds_read_b128 v[134:137], v169
	ds_read_b128 v[138:141], v170
	ds_read_b128 v[152:155], v171
	ds_read_b128 v[156:159], v172
	ds_read_b128 v[166:169], v173
	ds_read_b128 v[176:179], v173 offset:1024
	ds_read_b128 v[180:183], v173 offset:2048
	ds_read_b128 v[184:187], v173 offset:3072
	ds_read_b128 v[188:191], v173 offset:4096
	ds_read_b128 v[196:199], v173 offset:5120
	ds_read_b128 v[200:203], v173 offset:6144
	ds_read_b128 v[204:207], v173 offset:7168
	global_load_lds_dwordx4 v[130:131], off
	v_lshl_add_u64 v[130:131], v[132:133], 1, s[0:1]
	v_readfirstlane_b32 s0, v175
	s_mov_b32 m0, s0
	s_nop 0
	global_load_lds_dwordx4 v[130:131], off
	s_barrier
	s_waitcnt lgkmcnt(0)
	s_waitcnt lgkmcnt(0)
	v_mfma_f32_16x16x32_f16 v[2:5], v[166:169], v[134:137], v[2:5]
	v_mfma_f32_16x16x32_f16 v[42:45], v[188:191], v[152:155], v[42:45]
	v_mfma_f32_16x16x32_f16 v[54:57], v[200:203], v[134:137], v[54:57]
	v_mfma_f32_16x16x32_f16 v[66:69], v[200:203], v[152:155], v[66:69]
	v_mfma_f32_16x16x32_f16 v[2:5], v[176:179], v[138:141], v[2:5]
	v_mfma_f32_16x16x32_f16 v[6:9], v[166:169], v[152:155], v[6:9]
	v_mfma_f32_16x16x32_f16 v[10:13], v[180:183], v[134:137], v[10:13]
	v_mfma_f32_16x16x32_f16 v[18:21], v[180:183], v[152:155], v[18:21]
	v_mfma_f32_16x16x32_f16 v[30:33], v[188:191], v[134:137], v[30:33]
	v_mfma_f32_16x16x32_f16 v[42:45], v[196:199], v[156:159], v[42:45]
	v_mfma_f32_16x16x32_f16 v[54:57], v[204:207], v[138:141], v[54:57]
	v_mfma_f32_16x16x32_f16 v[66:69], v[204:207], v[156:159], v[66:69]
	v_mfma_f32_16x16x32_f16 v[6:9], v[176:179], v[156:159], v[6:9]
	v_mfma_f32_16x16x32_f16 v[10:13], v[184:187], v[138:141], v[10:13]
	v_mfma_f32_16x16x32_f16 v[18:21], v[184:187], v[156:159], v[18:21]
	v_mfma_f32_16x16x32_f16 v[30:33], v[196:199], v[138:141], v[30:33]
	s_barrier
	ds_read_b128 v[130:133], v161
	ds_read_b128 v[212:215], v162
	ds_read_b128 v[160:163], v163
	ds_read_b128 v[216:219], v164
	s_barrier
	s_waitcnt lgkmcnt(0)
	s_waitcnt lgkmcnt(0)
	v_mfma_f32_16x16x32_f16 v[14:17], v[166:169], v[130:133], v[14:17]
	v_mfma_f32_16x16x32_f16 v[78:81], v[200:203], v[130:133], v[78:81]
	v_mfma_f32_16x16x32_f16 v[14:17], v[176:179], v[212:215], v[14:17]
	v_mfma_f32_16x16x32_f16 v[22:25], v[166:169], v[160:163], v[22:25]
	v_mfma_f32_16x16x32_f16 v[34:37], v[180:183], v[130:133], v[34:37]
	v_mfma_f32_16x16x32_f16 v[46:49], v[180:183], v[160:163], v[46:49]
	v_mfma_f32_16x16x32_f16 v[58:61], v[188:191], v[130:133], v[58:61]
	v_mfma_f32_16x16x32_f16 v[70:73], v[188:191], v[160:163], v[70:73]
	v_mfma_f32_16x16x32_f16 v[164:167], v[204:207], v[212:215], v[78:81]
	v_mfma_f32_16x16x32_f16 v[78:81], v[200:203], v[160:163], v[86:89]
	v_mfma_f32_16x16x32_f16 v[22:25], v[176:179], v[216:219], v[22:25]
	v_mfma_f32_16x16x32_f16 v[34:37], v[184:187], v[212:215], v[34:37]
	v_mfma_f32_16x16x32_f16 v[46:49], v[184:187], v[216:219], v[46:49]
	v_mfma_f32_16x16x32_f16 v[58:61], v[196:199], v[212:215], v[58:61]
	v_mfma_f32_16x16x32_f16 v[70:73], v[196:199], v[216:219], v[70:73]
	v_mfma_f32_16x16x32_f16 v[86:89], v[204:207], v[216:219], v[78:81]
	s_barrier
	s_nop 0
	ds_read_b128 v[78:81], v173 offset:16384
	ds_read_b128 v[168:171], v173 offset:17408
	ds_read_b128 v[174:177], v173 offset:18432
	ds_read_b128 v[178:181], v173 offset:19456
	ds_read_b128 v[182:185], v173 offset:20480
	ds_read_b128 v[186:189], v173 offset:21504
	ds_read_b128 v[190:193], v173 offset:22528
	ds_read_b128 v[196:199], v173 offset:23552
	s_waitcnt vmcnt(4)
	s_barrier
	s_waitcnt lgkmcnt(0)
	s_waitcnt lgkmcnt(0)
	v_mfma_f32_16x16x32_f16 v[26:29], v[78:81], v[134:137], v[26:29]
	v_mfma_f32_16x16x32_f16 v[38:41], v[78:81], v[152:155], v[38:41]
	v_mfma_f32_16x16x32_f16 v[26:29], v[168:171], v[138:141], v[26:29]
	v_mfma_f32_16x16x32_f16 v[38:41], v[168:171], v[156:159], v[38:41]
	v_mfma_f32_16x16x32_f16 v[50:53], v[174:177], v[134:137], v[50:53]
	v_mfma_f32_16x16x32_f16 v[62:65], v[174:177], v[152:155], v[62:65]
	v_mfma_f32_16x16x32_f16 v[74:77], v[182:185], v[134:137], v[74:77]
	v_mfma_f32_16x16x32_f16 v[82:85], v[182:185], v[152:155], v[82:85]
	v_mfma_f32_16x16x32_f16 v[90:93], v[190:193], v[134:137], v[90:93]
	v_mfma_f32_16x16x32_f16 v[94:97], v[190:193], v[152:155], v[94:97]
	v_mfma_f32_16x16x32_f16 v[50:53], v[178:181], v[138:141], v[50:53]
	v_mfma_f32_16x16x32_f16 v[62:65], v[178:181], v[156:159], v[62:65]
	v_mfma_f32_16x16x32_f16 v[74:77], v[186:189], v[138:141], v[74:77]
	v_mfma_f32_16x16x32_f16 v[82:85], v[186:189], v[156:159], v[82:85]
	v_mfma_f32_16x16x32_f16 v[90:93], v[196:199], v[138:141], v[90:93]
	v_mfma_f32_16x16x32_f16 v[94:97], v[196:199], v[156:159], v[94:97]
	v_mfma_f32_16x16x32_f16 v[98:101], v[78:81], v[130:133], v[98:101]
	v_mfma_f32_16x16x32_f16 v[78:81], v[78:81], v[160:163], v[102:105]
	v_mfma_f32_16x16x32_f16 v[102:105], v[168:171], v[216:219], v[78:81]
	v_mfma_f32_16x16x32_f16 v[78:81], v[174:177], v[130:133], v[106:109]
	v_mfma_f32_16x16x32_f16 v[106:109], v[178:181], v[212:215], v[78:81]
	v_mfma_f32_16x16x32_f16 v[78:81], v[174:177], v[160:163], v[110:113]
	v_mfma_f32_16x16x32_f16 v[200:203], v[178:181], v[216:219], v[78:81]
	v_mfma_f32_16x16x32_f16 v[78:81], v[182:185], v[130:133], v[114:117]
	v_mfma_f32_16x16x32_f16 v[204:207], v[186:189], v[212:215], v[78:81]
	v_mfma_f32_16x16x32_f16 v[78:81], v[182:185], v[160:163], v[118:121]
	v_mfma_f32_16x16x32_f16 v[220:223], v[186:189], v[216:219], v[78:81]
	v_mfma_f32_16x16x32_f16 v[78:81], v[190:193], v[130:133], v[122:125]
	v_mfma_f32_16x16x32_f16 v[98:101], v[168:171], v[212:215], v[98:101]
	v_mfma_f32_16x16x32_f16 v[212:215], v[196:199], v[212:215], v[78:81]
	v_mfma_f32_16x16x32_f16 v[78:81], v[190:193], v[160:163], v[126:129]
	v_mfma_f32_16x16x32_f16 v[196:199], v[196:199], v[216:219], v[78:81]
	s_barrier
	ds_read_b128 v[110:113], v148
	ds_read_b128 v[130:133], v149
	ds_read_b128 v[216:219], v150
	ds_read_b128 v[224:227], v151
	s_nop 0
	ds_read_b128 v[78:81], v173 offset:32768
	ds_read_b128 v[114:117], v173 offset:33792
	ds_read_b128 v[118:121], v173 offset:34816
	ds_read_b128 v[134:137], v173 offset:35840
	ds_read_b128 v[138:141], v173 offset:36864
	ds_read_b128 v[168:171], v173 offset:37888
	ds_read_b128 v[174:177], v173 offset:38912
	ds_read_b128 v[228:231], v173 offset:39936
	s_waitcnt vmcnt(2)
	s_barrier
	s_waitcnt lgkmcnt(0)
	s_waitcnt lgkmcnt(0)
	v_mfma_f32_16x16x32_f16 v[2:5], v[78:81], v[110:113], v[2:5]
	v_mfma_f32_16x16x32_f16 v[190:193], v[114:117], v[130:133], v[2:5]
	v_mfma_f32_16x16x32_f16 v[2:5], v[78:81], v[216:219], v[6:9]
	v_mfma_f32_16x16x32_f16 v[158:161], v[114:117], v[224:227], v[2:5]
	v_mfma_f32_16x16x32_f16 v[2:5], v[118:121], v[110:113], v[10:13]
	v_mfma_f32_16x16x32_f16 v[186:189], v[134:137], v[130:133], v[2:5]
	v_mfma_f32_16x16x32_f16 v[2:5], v[118:121], v[216:219], v[18:21]
	v_mfma_f32_16x16x32_f16 v[154:157], v[134:137], v[224:227], v[2:5]
	v_mfma_f32_16x16x32_f16 v[2:5], v[138:141], v[110:113], v[30:33]
	v_mfma_f32_16x16x32_f16 v[182:185], v[168:171], v[130:133], v[2:5]
	v_mfma_f32_16x16x32_f16 v[2:5], v[138:141], v[216:219], v[42:45]
	v_mfma_f32_16x16x32_f16 v[150:153], v[168:171], v[224:227], v[2:5]
	v_mfma_f32_16x16x32_f16 v[2:5], v[174:177], v[110:113], v[54:57]
	v_mfma_f32_16x16x32_f16 v[178:181], v[228:231], v[130:133], v[2:5]
	v_mfma_f32_16x16x32_f16 v[2:5], v[174:177], v[216:219], v[66:69]
	v_mfma_f32_16x16x32_f16 v[146:149], v[228:231], v[224:227], v[2:5]
	s_barrier
	s_nop 4
	ds_read_b128 v[2:5], v142
	ds_read_b128 v[6:9], v143
	ds_read_b128 v[10:13], v144
	ds_read_b128 v[18:21], v145
	s_waitcnt vmcnt(0)
	s_barrier
	s_waitcnt lgkmcnt(0)
	s_waitcnt lgkmcnt(0)
	v_mfma_f32_16x16x32_f16 v[14:17], v[78:81], v[2:5], v[14:17]
	v_mfma_f32_16x16x32_f16 v[126:129], v[114:117], v[6:9], v[14:17]
	v_mfma_f32_16x16x32_f16 v[14:17], v[78:81], v[10:13], v[22:25]
	v_mfma_f32_16x16x32_f16 v[78:81], v[114:117], v[18:21], v[14:17]
	v_mfma_f32_16x16x32_f16 v[14:17], v[118:121], v[2:5], v[34:37]
	v_mfma_f32_16x16x32_f16 v[122:125], v[134:137], v[6:9], v[14:17]
	v_mfma_f32_16x16x32_f16 v[14:17], v[118:121], v[10:13], v[46:49]
	v_mfma_f32_16x16x32_f16 v[66:69], v[134:137], v[18:21], v[14:17]
	v_mfma_f32_16x16x32_f16 v[14:17], v[138:141], v[2:5], v[58:61]
	v_mfma_f32_16x16x32_f16 v[118:121], v[168:171], v[6:9], v[14:17]
	v_mfma_f32_16x16x32_f16 v[14:17], v[138:141], v[10:13], v[70:73]
	v_mfma_f32_16x16x32_f16 v[54:57], v[168:171], v[18:21], v[14:17]
	v_mfma_f32_16x16x32_f16 v[14:17], v[174:177], v[2:5], v[164:167]
	v_mfma_f32_16x16x32_f16 v[114:117], v[228:231], v[6:9], v[14:17]
	v_mfma_f32_16x16x32_f16 v[14:17], v[174:177], v[10:13], v[86:89]
	v_mfma_f32_16x16x32_f16 v[42:45], v[228:231], v[18:21], v[14:17]
	s_barrier
	s_nop 4
	ds_read_b128 v[14:17], v173 offset:49152
	ds_read_b128 v[22:25], v173 offset:50176
	ds_read_b128 v[30:33], v173 offset:51200
	ds_read_b128 v[34:37], v173 offset:52224
	ds_read_b128 v[46:49], v173 offset:53248
	ds_read_b128 v[58:61], v173 offset:54272
	ds_read_b128 v[70:73], v173 offset:55296
	ds_read_b128 v[86:89], v173 offset:56320
	s_barrier
	s_waitcnt lgkmcnt(0)
	s_waitcnt lgkmcnt(0)
	v_mfma_f32_16x16x32_f16 v[26:29], v[14:17], v[110:113], v[26:29]
	v_mfma_f32_16x16x32_f16 v[174:177], v[22:25], v[130:133], v[26:29]
	v_mfma_f32_16x16x32_f16 v[26:29], v[14:17], v[216:219], v[38:41]
	v_mfma_f32_16x16x32_f16 v[142:145], v[22:25], v[224:227], v[26:29]
	v_mfma_f32_16x16x32_f16 v[26:29], v[30:33], v[110:113], v[50:53]
	v_mfma_f32_16x16x32_f16 v[170:173], v[34:37], v[130:133], v[26:29]
	v_mfma_f32_16x16x32_f16 v[26:29], v[30:33], v[216:219], v[62:65]
	v_mfma_f32_16x16x32_f16 v[138:141], v[34:37], v[224:227], v[26:29]
	v_mfma_f32_16x16x32_f16 v[26:29], v[46:49], v[110:113], v[74:77]
	v_mfma_f32_16x16x32_f16 v[166:169], v[58:61], v[130:133], v[26:29]
	v_mfma_f32_16x16x32_f16 v[26:29], v[46:49], v[216:219], v[82:85]
	v_mfma_f32_16x16x32_f16 v[134:137], v[58:61], v[224:227], v[26:29]
	v_mfma_f32_16x16x32_f16 v[26:29], v[70:73], v[110:113], v[90:93]
	v_mfma_f32_16x16x32_f16 v[162:165], v[86:89], v[130:133], v[26:29]
	v_mfma_f32_16x16x32_f16 v[26:29], v[70:73], v[216:219], v[94:97]
	v_mfma_f32_16x16x32_f16 v[130:133], v[86:89], v[224:227], v[26:29]
	v_mfma_f32_16x16x32_f16 v[26:29], v[14:17], v[2:5], v[98:101]
	v_mfma_f32_16x16x32_f16 v[14:17], v[14:17], v[10:13], v[102:105]
	v_mfma_f32_16x16x32_f16 v[38:41], v[22:25], v[18:21], v[14:17]
	v_mfma_f32_16x16x32_f16 v[14:17], v[30:33], v[2:5], v[106:109]
	v_mfma_f32_16x16x32_f16 v[106:109], v[34:37], v[6:9], v[14:17]
	v_mfma_f32_16x16x32_f16 v[14:17], v[30:33], v[10:13], v[200:203]
	v_mfma_f32_16x16x32_f16 v[110:113], v[22:25], v[6:9], v[26:29]
	v_mfma_f32_16x16x32_f16 v[26:29], v[34:37], v[18:21], v[14:17]
	v_mfma_f32_16x16x32_f16 v[14:17], v[46:49], v[2:5], v[204:207]
	v_mfma_f32_16x16x32_f16 v[2:5], v[70:73], v[2:5], v[212:215]
	v_mfma_f32_16x16x32_f16 v[102:105], v[58:61], v[6:9], v[14:17]
	v_mfma_f32_16x16x32_f16 v[14:17], v[46:49], v[10:13], v[220:223]
	v_mfma_f32_16x16x32_f16 v[98:101], v[86:89], v[6:9], v[2:5]
	v_mfma_f32_16x16x32_f16 v[2:5], v[70:73], v[10:13], v[196:199]
	v_mfma_f32_16x16x32_f16 v[14:17], v[58:61], v[18:21], v[14:17]
	v_mfma_f32_16x16x32_f16 v[2:5], v[86:89], v[18:21], v[2:5]
	s_cmpk_gt_u32 s65, 0xff
	s_barrier
	s_cbranch_scc1 .LBB6_15
	s_barrier

.LBB7_239:
	ds_read_b128 v[176:179], v169
	ds_read_b128 v[180:183], v170
	ds_read_b128 v[184:187], v171
	ds_read_b128 v[188:191], v172
	v_add_u32_e32 v174, 0xc000, v152
	v_lshl_add_u64 v[192:193], v[136:137], 0, s[46:47]
	v_readfirstlane_b32 s49, v174
	v_add_u32_e32 v175, 0xe000, v152
	v_add_u32_e32 v173, s5, v168
	v_lshl_add_u64 v[232:233], v[192:193], 0, s[34:35]
	s_mov_b32 m0, s49
	v_lshl_add_u64 v[248:249], v[134:135], 0, s[46:47]
	v_readfirstlane_b32 s49, v175
	ds_read_b128 v[196:199], v173
	ds_read_b128 v[200:203], v173 offset:1024
	ds_read_b128 v[204:207], v173 offset:2048
	ds_read_b128 v[212:215], v173 offset:3072
	ds_read_b128 v[216:219], v173 offset:4096
	ds_read_b128 v[220:223], v173 offset:5120
	ds_read_b128 v[224:227], v173 offset:6144
	ds_read_b128 v[228:231], v173 offset:7168
	global_load_lds_dwordx4 v[232:233], off
	v_lshl_add_u64 v[232:233], v[248:249], 0, s[34:35]
	s_mov_b32 m0, s49
	s_nop 0
	global_load_lds_dwordx4 v[232:233], off
	s_waitcnt lgkmcnt(8)
	s_barrier
	s_waitcnt lgkmcnt(0)
	s_waitcnt lgkmcnt(0)
	v_mfma_f32_16x16x32_f16 v[2:5], v[196:199], v[176:179], v[2:5]
	v_mfma_f32_16x16x32_f16 v[6:9], v[196:199], v[184:187], v[6:9]
	v_mfma_f32_16x16x32_f16 v[10:13], v[204:207], v[176:179], v[10:13]
	v_mfma_f32_16x16x32_f16 v[18:21], v[204:207], v[184:187], v[18:21]
	v_mfma_f32_16x16x32_f16 v[30:33], v[216:219], v[176:179], v[30:33]
	v_mfma_f32_16x16x32_f16 v[42:45], v[216:219], v[184:187], v[42:45]
	v_mfma_f32_16x16x32_f16 v[54:57], v[224:227], v[176:179], v[54:57]
	v_mfma_f32_16x16x32_f16 v[66:69], v[224:227], v[184:187], v[66:69]
	v_mfma_f32_16x16x32_f16 v[2:5], v[200:203], v[180:183], v[2:5]
	v_mfma_f32_16x16x32_f16 v[6:9], v[200:203], v[188:191], v[6:9]
	v_mfma_f32_16x16x32_f16 v[10:13], v[212:215], v[180:183], v[10:13]
	v_mfma_f32_16x16x32_f16 v[18:21], v[212:215], v[188:191], v[18:21]
	v_mfma_f32_16x16x32_f16 v[30:33], v[220:223], v[180:183], v[30:33]
	v_mfma_f32_16x16x32_f16 v[42:45], v[220:223], v[188:191], v[42:45]
	v_mfma_f32_16x16x32_f16 v[54:57], v[228:231], v[180:183], v[54:57]
	v_mfma_f32_16x16x32_f16 v[66:69], v[228:231], v[188:191], v[66:69]
	s_barrier
	v_lshl_add_u64 v[250:251], v[140:141], 0, s[46:47]
	v_readfirstlane_b32 s49, v146
	v_lshl_add_u64 v[252:253], v[250:251], 0, s[36:37]
	s_mov_b32 m0, s49
	ds_read_b128 v[232:235], v161
	ds_read_b128 v[236:239], v162
	ds_read_b128 v[240:243], v163
	ds_read_b128 v[244:247], v164
	global_load_lds_dwordx4 v[252:253], off
	v_lshl_add_u64 v[252:253], v[138:139], 0, s[46:47]
	v_readfirstlane_b32 s49, v147
	v_lshl_add_u64 v[254:255], v[252:253], 0, s[36:37]
	s_mov_b32 m0, s49
	s_nop 0
	global_load_lds_dwordx4 v[254:255], off
	s_barrier
	s_waitcnt lgkmcnt(0)
	s_waitcnt lgkmcnt(0)
	v_mfma_f32_16x16x32_f16 v[14:17], v[196:199], v[232:235], v[14:17]
	v_mfma_f32_16x16x32_f16 v[22:25], v[196:199], v[240:243], v[22:25]
	v_mfma_f32_16x16x32_f16 v[34:37], v[204:207], v[232:235], v[34:37]
	v_mfma_f32_16x16x32_f16 v[46:49], v[204:207], v[240:243], v[46:49]
	v_mfma_f32_16x16x32_f16 v[58:61], v[216:219], v[232:235], v[58:61]
	v_mfma_f32_16x16x32_f16 v[70:73], v[216:219], v[240:243], v[70:73]
	v_mfma_f32_16x16x32_f16 v[78:81], v[224:227], v[232:235], v[78:81]
	v_mfma_f32_16x16x32_f16 v[86:89], v[224:227], v[240:243], v[86:89]
	v_mfma_f32_16x16x32_f16 v[14:17], v[200:203], v[236:239], v[14:17]
	v_mfma_f32_16x16x32_f16 v[22:25], v[200:203], v[244:247], v[22:25]
	v_mfma_f32_16x16x32_f16 v[34:37], v[212:215], v[236:239], v[34:37]
	v_mfma_f32_16x16x32_f16 v[46:49], v[212:215], v[244:247], v[46:49]
	v_mfma_f32_16x16x32_f16 v[58:61], v[220:223], v[236:239], v[58:61]
	v_mfma_f32_16x16x32_f16 v[70:73], v[220:223], v[244:247], v[70:73]
	v_mfma_f32_16x16x32_f16 v[78:81], v[228:231], v[236:239], v[78:81]
	v_mfma_f32_16x16x32_f16 v[86:89], v[228:231], v[244:247], v[86:89]
	v_readfirstlane_b32 s49, v152
	v_lshl_add_u64 v[254:255], v[192:193], 0, s[36:37]
	s_mov_b32 m0, s49
	v_readfirstlane_b32 s49, v153
	s_barrier
	ds_read_b128 v[196:199], v173 offset:16384
	ds_read_b128 v[200:203], v173 offset:17408
	ds_read_b128 v[204:207], v173 offset:18432
	ds_read_b128 v[212:215], v173 offset:19456
	ds_read_b128 v[216:219], v173 offset:20480
	ds_read_b128 v[220:223], v173 offset:21504
	ds_read_b128 v[224:227], v173 offset:22528
	ds_read_b128 v[228:231], v173 offset:23552
	global_load_lds_dwordx4 v[254:255], off
	v_lshl_add_u64 v[254:255], v[248:249], 0, s[36:37]
	s_mov_b32 m0, s49
	s_nop 0
	global_load_lds_dwordx4 v[254:255], off
	s_barrier
	s_waitcnt lgkmcnt(0)
	s_waitcnt lgkmcnt(0)
	v_mfma_f32_16x16x32_f16 v[26:29], v[196:199], v[176:179], v[26:29]
	v_mfma_f32_16x16x32_f16 v[38:41], v[196:199], v[184:187], v[38:41]
	v_mfma_f32_16x16x32_f16 v[50:53], v[204:207], v[176:179], v[50:53]
	v_mfma_f32_16x16x32_f16 v[62:65], v[204:207], v[184:187], v[62:65]
	v_mfma_f32_16x16x32_f16 v[74:77], v[216:219], v[176:179], v[74:77]
	v_mfma_f32_16x16x32_f16 v[82:85], v[216:219], v[184:187], v[82:85]
	v_mfma_f32_16x16x32_f16 v[90:93], v[224:227], v[176:179], v[90:93]
	v_mfma_f32_16x16x32_f16 v[94:97], v[224:227], v[184:187], v[94:97]
	v_mfma_f32_16x16x32_f16 v[26:29], v[200:203], v[180:183], v[26:29]
	v_mfma_f32_16x16x32_f16 v[38:41], v[200:203], v[188:191], v[38:41]
	v_mfma_f32_16x16x32_f16 v[50:53], v[212:215], v[180:183], v[50:53]
	v_mfma_f32_16x16x32_f16 v[62:65], v[212:215], v[188:191], v[62:65]
	v_mfma_f32_16x16x32_f16 v[74:77], v[220:223], v[180:183], v[74:77]
	v_mfma_f32_16x16x32_f16 v[82:85], v[220:223], v[188:191], v[82:85]
	v_mfma_f32_16x16x32_f16 v[90:93], v[228:231], v[180:183], v[90:93]
	v_mfma_f32_16x16x32_f16 v[94:97], v[228:231], v[188:191], v[94:97]
	s_barrier
	v_readfirstlane_b32 s49, v154
	v_lshl_add_u64 v[176:177], v[250:251], 0, s[38:39]
	s_mov_b32 m0, s49
	v_readfirstlane_b32 s49, v155
	global_load_lds_dwordx4 v[176:177], off
	v_lshl_add_u64 v[176:177], v[252:253], 0, s[38:39]
	s_mov_b32 m0, s49
	s_nop 0
	global_load_lds_dwordx4 v[176:177], off
	s_waitcnt vmcnt(6)
	s_barrier
	v_mfma_f32_16x16x32_f16 v[98:101], v[196:199], v[232:235], v[98:101]
	v_mfma_f32_16x16x32_f16 v[102:105], v[196:199], v[240:243], v[102:105]
	v_mfma_f32_16x16x32_f16 v[106:109], v[204:207], v[232:235], v[106:109]
	v_mfma_f32_16x16x32_f16 v[110:113], v[204:207], v[240:243], v[110:113]
	v_mfma_f32_16x16x32_f16 v[114:117], v[216:219], v[232:235], v[114:117]
	v_mfma_f32_16x16x32_f16 v[118:121], v[216:219], v[240:243], v[118:121]
	v_mfma_f32_16x16x32_f16 v[122:125], v[224:227], v[232:235], v[122:125]
	v_mfma_f32_16x16x32_f16 v[126:129], v[224:227], v[240:243], v[126:129]
	v_mfma_f32_16x16x32_f16 v[98:101], v[200:203], v[236:239], v[98:101]
	v_mfma_f32_16x16x32_f16 v[102:105], v[200:203], v[244:247], v[102:105]
	v_mfma_f32_16x16x32_f16 v[106:109], v[212:215], v[236:239], v[106:109]
	v_mfma_f32_16x16x32_f16 v[110:113], v[212:215], v[244:247], v[110:113]
	v_mfma_f32_16x16x32_f16 v[114:117], v[220:223], v[236:239], v[114:117]
	v_mfma_f32_16x16x32_f16 v[118:121], v[220:223], v[244:247], v[118:121]
	v_mfma_f32_16x16x32_f16 v[122:125], v[228:231], v[236:239], v[122:125]
	v_mfma_f32_16x16x32_f16 v[126:129], v[228:231], v[244:247], v[126:129]
	s_barrier
	ds_read_b128 v[176:179], v148
	ds_read_b128 v[180:183], v149
	ds_read_b128 v[184:187], v150
	ds_read_b128 v[188:191], v151
	v_readfirstlane_b32 s49, v156
	v_lshl_add_u64 v[232:233], v[192:193], 0, s[38:39]
	s_mov_b32 m0, s49
	v_readfirstlane_b32 s49, v157
	ds_read_b128 v[196:199], v173 offset:32768
	ds_read_b128 v[200:203], v173 offset:33792
	ds_read_b128 v[204:207], v173 offset:34816
	ds_read_b128 v[212:215], v173 offset:35840
	ds_read_b128 v[216:219], v173 offset:36864
	ds_read_b128 v[220:223], v173 offset:37888
	ds_read_b128 v[224:227], v173 offset:38912
	ds_read_b128 v[228:231], v173 offset:39936
	global_load_lds_dwordx4 v[232:233], off
	v_lshl_add_u64 v[232:233], v[248:249], 0, s[38:39]
	s_mov_b32 m0, s49
	s_nop 0
	global_load_lds_dwordx4 v[232:233], off
	s_waitcnt lgkmcnt(8)
	s_barrier
	s_waitcnt lgkmcnt(0)
	s_waitcnt lgkmcnt(0)
	v_mfma_f32_16x16x32_f16 v[2:5], v[196:199], v[176:179], v[2:5]
	v_mfma_f32_16x16x32_f16 v[6:9], v[196:199], v[184:187], v[6:9]
	v_mfma_f32_16x16x32_f16 v[10:13], v[204:207], v[176:179], v[10:13]
	v_mfma_f32_16x16x32_f16 v[18:21], v[204:207], v[184:187], v[18:21]
	v_mfma_f32_16x16x32_f16 v[30:33], v[216:219], v[176:179], v[30:33]
	v_mfma_f32_16x16x32_f16 v[42:45], v[216:219], v[184:187], v[42:45]
	v_mfma_f32_16x16x32_f16 v[54:57], v[224:227], v[176:179], v[54:57]
	v_mfma_f32_16x16x32_f16 v[66:69], v[224:227], v[184:187], v[66:69]
	v_mfma_f32_16x16x32_f16 v[2:5], v[200:203], v[180:183], v[2:5]
	v_mfma_f32_16x16x32_f16 v[6:9], v[200:203], v[188:191], v[6:9]
	v_mfma_f32_16x16x32_f16 v[10:13], v[212:215], v[180:183], v[10:13]
	v_mfma_f32_16x16x32_f16 v[18:21], v[212:215], v[188:191], v[18:21]
	v_mfma_f32_16x16x32_f16 v[30:33], v[220:223], v[180:183], v[30:33]
	v_mfma_f32_16x16x32_f16 v[42:45], v[220:223], v[188:191], v[42:45]
	v_mfma_f32_16x16x32_f16 v[54:57], v[228:231], v[180:183], v[54:57]
	v_mfma_f32_16x16x32_f16 v[66:69], v[228:231], v[188:191], v[66:69]
	s_barrier
	v_readfirstlane_b32 s49, v158
	v_lshl_add_u64 v[254:255], v[250:251], 0, s[40:41]
	s_mov_b32 m0, s49
	v_readfirstlane_b32 s49, v159
	ds_read_b128 v[232:235], v142
	ds_read_b128 v[236:239], v143
	ds_read_b128 v[240:243], v144
	ds_read_b128 v[244:247], v145
	global_load_lds_dwordx4 v[254:255], off
	v_lshl_add_u64 v[254:255], v[252:253], 0, s[40:41]
	s_mov_b32 m0, s49
	s_nop 0
	global_load_lds_dwordx4 v[254:255], off
	s_barrier
	s_waitcnt lgkmcnt(0)
	s_waitcnt lgkmcnt(0)
	v_mfma_f32_16x16x32_f16 v[14:17], v[196:199], v[232:235], v[14:17]
	v_mfma_f32_16x16x32_f16 v[22:25], v[196:199], v[240:243], v[22:25]
	v_mfma_f32_16x16x32_f16 v[34:37], v[204:207], v[232:235], v[34:37]
	v_mfma_f32_16x16x32_f16 v[46:49], v[204:207], v[240:243], v[46:49]
	v_mfma_f32_16x16x32_f16 v[58:61], v[216:219], v[232:235], v[58:61]
	v_mfma_f32_16x16x32_f16 v[70:73], v[216:219], v[240:243], v[70:73]
	v_mfma_f32_16x16x32_f16 v[78:81], v[224:227], v[232:235], v[78:81]
	v_mfma_f32_16x16x32_f16 v[86:89], v[224:227], v[240:243], v[86:89]
	v_mfma_f32_16x16x32_f16 v[14:17], v[200:203], v[236:239], v[14:17]
	v_mfma_f32_16x16x32_f16 v[22:25], v[200:203], v[244:247], v[22:25]
	v_mfma_f32_16x16x32_f16 v[34:37], v[212:215], v[236:239], v[34:37]
	v_mfma_f32_16x16x32_f16 v[46:49], v[212:215], v[244:247], v[46:49]
	v_mfma_f32_16x16x32_f16 v[58:61], v[220:223], v[236:239], v[58:61]
	v_mfma_f32_16x16x32_f16 v[70:73], v[220:223], v[244:247], v[70:73]
	v_mfma_f32_16x16x32_f16 v[78:81], v[228:231], v[236:239], v[78:81]
	v_mfma_f32_16x16x32_f16 v[86:89], v[228:231], v[244:247], v[86:89]
	v_readfirstlane_b32 s49, v160
	v_lshl_add_u64 v[192:193], v[192:193], 0, s[40:41]
	s_mov_b32 m0, s49
	v_readfirstlane_b32 s49, v165
	s_barrier
	ds_read_b128 v[196:199], v173 offset:49152
	ds_read_b128 v[200:203], v173 offset:50176
	ds_read_b128 v[204:207], v173 offset:51200
	ds_read_b128 v[212:215], v173 offset:52224
	ds_read_b128 v[216:219], v173 offset:53248
	ds_read_b128 v[220:223], v173 offset:54272
	ds_read_b128 v[224:227], v173 offset:55296
	ds_read_b128 v[228:231], v173 offset:56320
	global_load_lds_dwordx4 v[192:193], off
	v_lshl_add_u64 v[192:193], v[248:249], 0, s[40:41]
	s_mov_b32 m0, s49
	s_nop 0
	global_load_lds_dwordx4 v[192:193], off
	s_barrier
	s_waitcnt lgkmcnt(0)
	s_waitcnt lgkmcnt(0)
	v_mfma_f32_16x16x32_f16 v[26:29], v[196:199], v[176:179], v[26:29]
	v_mfma_f32_16x16x32_f16 v[38:41], v[196:199], v[184:187], v[38:41]
	v_mfma_f32_16x16x32_f16 v[50:53], v[204:207], v[176:179], v[50:53]
	v_mfma_f32_16x16x32_f16 v[62:65], v[204:207], v[184:187], v[62:65]
	v_mfma_f32_16x16x32_f16 v[74:77], v[216:219], v[176:179], v[74:77]
	v_mfma_f32_16x16x32_f16 v[82:85], v[216:219], v[184:187], v[82:85]
	v_mfma_f32_16x16x32_f16 v[90:93], v[224:227], v[176:179], v[90:93]
	v_mfma_f32_16x16x32_f16 v[94:97], v[224:227], v[184:187], v[94:97]
	v_mfma_f32_16x16x32_f16 v[26:29], v[200:203], v[180:183], v[26:29]
	v_mfma_f32_16x16x32_f16 v[38:41], v[200:203], v[188:191], v[38:41]
	v_mfma_f32_16x16x32_f16 v[50:53], v[212:215], v[180:183], v[50:53]
	v_mfma_f32_16x16x32_f16 v[62:65], v[212:215], v[188:191], v[62:65]
	v_mfma_f32_16x16x32_f16 v[74:77], v[220:223], v[180:183], v[74:77]
	v_mfma_f32_16x16x32_f16 v[82:85], v[220:223], v[188:191], v[82:85]
	v_mfma_f32_16x16x32_f16 v[90:93], v[228:231], v[180:183], v[90:93]
	v_mfma_f32_16x16x32_f16 v[94:97], v[228:231], v[188:191], v[94:97]
	s_barrier
	v_readfirstlane_b32 s49, v166
	v_lshl_add_u64 v[176:177], v[250:251], 0, s[42:43]
	s_mov_b32 m0, s49
	v_readfirstlane_b32 s49, v167
	global_load_lds_dwordx4 v[176:177], off
	v_lshl_add_u64 v[176:177], v[252:253], 0, s[42:43]
	s_mov_b32 m0, s49
	s_nop 0
	global_load_lds_dwordx4 v[176:177], off
	s_waitcnt vmcnt(6)
	s_barrier
	v_mfma_f32_16x16x32_f16 v[98:101], v[196:199], v[232:235], v[98:101]
	v_mfma_f32_16x16x32_f16 v[102:105], v[196:199], v[240:243], v[102:105]
	v_mfma_f32_16x16x32_f16 v[106:109], v[204:207], v[232:235], v[106:109]
	v_mfma_f32_16x16x32_f16 v[110:113], v[204:207], v[240:243], v[110:113]
	v_mfma_f32_16x16x32_f16 v[114:117], v[216:219], v[232:235], v[114:117]
	v_mfma_f32_16x16x32_f16 v[118:121], v[216:219], v[240:243], v[118:121]
	v_mfma_f32_16x16x32_f16 v[122:125], v[224:227], v[232:235], v[122:125]
	v_mfma_f32_16x16x32_f16 v[126:129], v[224:227], v[240:243], v[126:129]
	v_mfma_f32_16x16x32_f16 v[98:101], v[200:203], v[236:239], v[98:101]
	v_mfma_f32_16x16x32_f16 v[102:105], v[200:203], v[244:247], v[102:105]
	v_mfma_f32_16x16x32_f16 v[106:109], v[212:215], v[236:239], v[106:109]
	v_mfma_f32_16x16x32_f16 v[110:113], v[212:215], v[244:247], v[110:113]
	v_mfma_f32_16x16x32_f16 v[114:117], v[220:223], v[236:239], v[114:117]
	v_mfma_f32_16x16x32_f16 v[118:121], v[220:223], v[244:247], v[118:121]
	v_mfma_f32_16x16x32_f16 v[122:125], v[228:231], v[236:239], v[122:125]
	v_mfma_f32_16x16x32_f16 v[126:129], v[228:231], v[244:247], v[126:129]
	s_add_i32 s48, s48, 2
	s_add_u32 s46, s46, 0x100
	s_addc_u32 s47, s47, 0
	s_cmp_lt_u32 s48, 4
	s_barrier
	s_cbranch_scc1 .LBB7_239
	s_add_u32 s0, s0, 0x20380
	s_addc_u32 s1, s1, 0
	v_readfirstlane_b32 s5, v174
	v_lshl_add_u64 v[130:131], v[130:131], 1, s[0:1]
	s_mov_b32 m0, s5
	ds_read_b128 v[134:137], v169
	ds_read_b128 v[138:141], v170
	ds_read_b128 v[152:155], v171
	ds_read_b128 v[156:159], v172
	ds_read_b128 v[166:169], v173
	ds_read_b128 v[176:179], v173 offset:1024
	ds_read_b128 v[180:183], v173 offset:2048
	ds_read_b128 v[184:187], v173 offset:3072
	ds_read_b128 v[188:191], v173 offset:4096
	ds_read_b128 v[196:199], v173 offset:5120
	ds_read_b128 v[200:203], v173 offset:6144
	ds_read_b128 v[204:207], v173 offset:7168
	global_load_lds_dwordx4 v[130:131], off
	v_lshl_add_u64 v[130:131], v[132:133], 1, s[0:1]
	v_readfirstlane_b32 s0, v175
	s_mov_b32 m0, s0
	s_nop 0
	global_load_lds_dwordx4 v[130:131], off
	s_barrier
	s_waitcnt lgkmcnt(0)
	s_waitcnt lgkmcnt(0)
	v_mfma_f32_16x16x32_f16 v[2:5], v[166:169], v[134:137], v[2:5]
	v_mfma_f32_16x16x32_f16 v[42:45], v[188:191], v[152:155], v[42:45]
	v_mfma_f32_16x16x32_f16 v[54:57], v[200:203], v[134:137], v[54:57]
	v_mfma_f32_16x16x32_f16 v[66:69], v[200:203], v[152:155], v[66:69]
	v_mfma_f32_16x16x32_f16 v[2:5], v[176:179], v[138:141], v[2:5]
	v_mfma_f32_16x16x32_f16 v[6:9], v[166:169], v[152:155], v[6:9]
	v_mfma_f32_16x16x32_f16 v[10:13], v[180:183], v[134:137], v[10:13]
	v_mfma_f32_16x16x32_f16 v[18:21], v[180:183], v[152:155], v[18:21]
	v_mfma_f32_16x16x32_f16 v[30:33], v[188:191], v[134:137], v[30:33]
	v_mfma_f32_16x16x32_f16 v[42:45], v[196:199], v[156:159], v[42:45]
	v_mfma_f32_16x16x32_f16 v[54:57], v[204:207], v[138:141], v[54:57]
	v_mfma_f32_16x16x32_f16 v[66:69], v[204:207], v[156:159], v[66:69]
	v_mfma_f32_16x16x32_f16 v[6:9], v[176:179], v[156:159], v[6:9]
	v_mfma_f32_16x16x32_f16 v[10:13], v[184:187], v[138:141], v[10:13]
	v_mfma_f32_16x16x32_f16 v[18:21], v[184:187], v[156:159], v[18:21]
	v_mfma_f32_16x16x32_f16 v[30:33], v[196:199], v[138:141], v[30:33]
	s_barrier
	ds_read_b128 v[130:133], v161
	ds_read_b128 v[212:215], v162
	ds_read_b128 v[160:163], v163
	ds_read_b128 v[216:219], v164
	s_barrier
	s_waitcnt lgkmcnt(0)
	s_waitcnt lgkmcnt(0)
	v_mfma_f32_16x16x32_f16 v[14:17], v[166:169], v[130:133], v[14:17]
	v_mfma_f32_16x16x32_f16 v[78:81], v[200:203], v[130:133], v[78:81]
	v_mfma_f32_16x16x32_f16 v[14:17], v[176:179], v[212:215], v[14:17]
	v_mfma_f32_16x16x32_f16 v[22:25], v[166:169], v[160:163], v[22:25]
	v_mfma_f32_16x16x32_f16 v[34:37], v[180:183], v[130:133], v[34:37]
	v_mfma_f32_16x16x32_f16 v[46:49], v[180:183], v[160:163], v[46:49]
	v_mfma_f32_16x16x32_f16 v[58:61], v[188:191], v[130:133], v[58:61]
	v_mfma_f32_16x16x32_f16 v[70:73], v[188:191], v[160:163], v[70:73]
	v_mfma_f32_16x16x32_f16 v[164:167], v[204:207], v[212:215], v[78:81]
	v_mfma_f32_16x16x32_f16 v[78:81], v[200:203], v[160:163], v[86:89]
	v_mfma_f32_16x16x32_f16 v[22:25], v[176:179], v[216:219], v[22:25]
	v_mfma_f32_16x16x32_f16 v[34:37], v[184:187], v[212:215], v[34:37]
	v_mfma_f32_16x16x32_f16 v[46:49], v[184:187], v[216:219], v[46:49]
	v_mfma_f32_16x16x32_f16 v[58:61], v[196:199], v[212:215], v[58:61]
	v_mfma_f32_16x16x32_f16 v[70:73], v[196:199], v[216:219], v[70:73]
	v_mfma_f32_16x16x32_f16 v[86:89], v[204:207], v[216:219], v[78:81]
	s_barrier
	s_nop 0
	ds_read_b128 v[78:81], v173 offset:16384
	ds_read_b128 v[168:171], v173 offset:17408
	ds_read_b128 v[174:177], v173 offset:18432
	ds_read_b128 v[178:181], v173 offset:19456
	ds_read_b128 v[182:185], v173 offset:20480
	ds_read_b128 v[186:189], v173 offset:21504
	ds_read_b128 v[190:193], v173 offset:22528
	ds_read_b128 v[196:199], v173 offset:23552
	s_waitcnt vmcnt(4)
	s_barrier
	s_waitcnt lgkmcnt(0)
	s_waitcnt lgkmcnt(0)
	v_mfma_f32_16x16x32_f16 v[26:29], v[78:81], v[134:137], v[26:29]
	v_mfma_f32_16x16x32_f16 v[38:41], v[78:81], v[152:155], v[38:41]
	v_mfma_f32_16x16x32_f16 v[26:29], v[168:171], v[138:141], v[26:29]
	v_mfma_f32_16x16x32_f16 v[38:41], v[168:171], v[156:159], v[38:41]
	v_mfma_f32_16x16x32_f16 v[50:53], v[174:177], v[134:137], v[50:53]
	v_mfma_f32_16x16x32_f16 v[62:65], v[174:177], v[152:155], v[62:65]
	v_mfma_f32_16x16x32_f16 v[74:77], v[182:185], v[134:137], v[74:77]
	v_mfma_f32_16x16x32_f16 v[82:85], v[182:185], v[152:155], v[82:85]
	v_mfma_f32_16x16x32_f16 v[90:93], v[190:193], v[134:137], v[90:93]
	v_mfma_f32_16x16x32_f16 v[94:97], v[190:193], v[152:155], v[94:97]
	v_mfma_f32_16x16x32_f16 v[50:53], v[178:181], v[138:141], v[50:53]
	v_mfma_f32_16x16x32_f16 v[62:65], v[178:181], v[156:159], v[62:65]
	v_mfma_f32_16x16x32_f16 v[74:77], v[186:189], v[138:141], v[74:77]
	v_mfma_f32_16x16x32_f16 v[82:85], v[186:189], v[156:159], v[82:85]
	v_mfma_f32_16x16x32_f16 v[90:93], v[196:199], v[138:141], v[90:93]
	v_mfma_f32_16x16x32_f16 v[94:97], v[196:199], v[156:159], v[94:97]
	v_mfma_f32_16x16x32_f16 v[98:101], v[78:81], v[130:133], v[98:101]
	v_mfma_f32_16x16x32_f16 v[78:81], v[78:81], v[160:163], v[102:105]
	v_mfma_f32_16x16x32_f16 v[102:105], v[168:171], v[216:219], v[78:81]
	v_mfma_f32_16x16x32_f16 v[78:81], v[174:177], v[130:133], v[106:109]
	v_mfma_f32_16x16x32_f16 v[106:109], v[178:181], v[212:215], v[78:81]
	v_mfma_f32_16x16x32_f16 v[78:81], v[174:177], v[160:163], v[110:113]
	v_mfma_f32_16x16x32_f16 v[200:203], v[178:181], v[216:219], v[78:81]
	v_mfma_f32_16x16x32_f16 v[78:81], v[182:185], v[130:133], v[114:117]
	v_mfma_f32_16x16x32_f16 v[204:207], v[186:189], v[212:215], v[78:81]
	v_mfma_f32_16x16x32_f16 v[78:81], v[182:185], v[160:163], v[118:121]
	v_mfma_f32_16x16x32_f16 v[220:223], v[186:189], v[216:219], v[78:81]
	v_mfma_f32_16x16x32_f16 v[78:81], v[190:193], v[130:133], v[122:125]
	v_mfma_f32_16x16x32_f16 v[98:101], v[168:171], v[212:215], v[98:101]
	v_mfma_f32_16x16x32_f16 v[212:215], v[196:199], v[212:215], v[78:81]
	v_mfma_f32_16x16x32_f16 v[78:81], v[190:193], v[160:163], v[126:129]
	v_mfma_f32_16x16x32_f16 v[196:199], v[196:199], v[216:219], v[78:81]
	s_barrier
	ds_read_b128 v[110:113], v148
	ds_read_b128 v[130:133], v149
	ds_read_b128 v[216:219], v150
	ds_read_b128 v[224:227], v151
	s_nop 0
	ds_read_b128 v[78:81], v173 offset:32768
	ds_read_b128 v[114:117], v173 offset:33792
	ds_read_b128 v[118:121], v173 offset:34816
	ds_read_b128 v[134:137], v173 offset:35840
	ds_read_b128 v[138:141], v173 offset:36864
	ds_read_b128 v[168:171], v173 offset:37888
	ds_read_b128 v[174:177], v173 offset:38912
	ds_read_b128 v[228:231], v173 offset:39936
	s_waitcnt vmcnt(2)
	s_barrier
	s_waitcnt lgkmcnt(0)
	s_waitcnt lgkmcnt(0)
	v_mfma_f32_16x16x32_f16 v[2:5], v[78:81], v[110:113], v[2:5]
	v_mfma_f32_16x16x32_f16 v[190:193], v[114:117], v[130:133], v[2:5]
	v_mfma_f32_16x16x32_f16 v[2:5], v[78:81], v[216:219], v[6:9]
	v_mfma_f32_16x16x32_f16 v[158:161], v[114:117], v[224:227], v[2:5]
	v_mfma_f32_16x16x32_f16 v[2:5], v[118:121], v[110:113], v[10:13]
	v_mfma_f32_16x16x32_f16 v[186:189], v[134:137], v[130:133], v[2:5]
	v_mfma_f32_16x16x32_f16 v[2:5], v[118:121], v[216:219], v[18:21]
	v_mfma_f32_16x16x32_f16 v[154:157], v[134:137], v[224:227], v[2:5]
	v_mfma_f32_16x16x32_f16 v[2:5], v[138:141], v[110:113], v[30:33]
	v_mfma_f32_16x16x32_f16 v[182:185], v[168:171], v[130:133], v[2:5]
	v_mfma_f32_16x16x32_f16 v[2:5], v[138:141], v[216:219], v[42:45]
	v_mfma_f32_16x16x32_f16 v[150:153], v[168:171], v[224:227], v[2:5]
	v_mfma_f32_16x16x32_f16 v[2:5], v[174:177], v[110:113], v[54:57]
	v_mfma_f32_16x16x32_f16 v[178:181], v[228:231], v[130:133], v[2:5]
	v_mfma_f32_16x16x32_f16 v[2:5], v[174:177], v[216:219], v[66:69]
	v_mfma_f32_16x16x32_f16 v[146:149], v[228:231], v[224:227], v[2:5]
	s_barrier
	s_nop 4
	ds_read_b128 v[2:5], v142
	ds_read_b128 v[6:9], v143
	ds_read_b128 v[10:13], v144
	ds_read_b128 v[18:21], v145
	s_waitcnt vmcnt(0)
	s_barrier
	s_waitcnt lgkmcnt(0)
	s_waitcnt lgkmcnt(0)
	v_mfma_f32_16x16x32_f16 v[14:17], v[78:81], v[2:5], v[14:17]
	v_mfma_f32_16x16x32_f16 v[126:129], v[114:117], v[6:9], v[14:17]
	v_mfma_f32_16x16x32_f16 v[14:17], v[78:81], v[10:13], v[22:25]
	v_mfma_f32_16x16x32_f16 v[78:81], v[114:117], v[18:21], v[14:17]
	v_mfma_f32_16x16x32_f16 v[14:17], v[118:121], v[2:5], v[34:37]
	v_mfma_f32_16x16x32_f16 v[122:125], v[134:137], v[6:9], v[14:17]
	v_mfma_f32_16x16x32_f16 v[14:17], v[118:121], v[10:13], v[46:49]
	v_mfma_f32_16x16x32_f16 v[66:69], v[134:137], v[18:21], v[14:17]
	v_mfma_f32_16x16x32_f16 v[14:17], v[138:141], v[2:5], v[58:61]
	v_mfma_f32_16x16x32_f16 v[118:121], v[168:171], v[6:9], v[14:17]
	v_mfma_f32_16x16x32_f16 v[14:17], v[138:141], v[10:13], v[70:73]
	v_mfma_f32_16x16x32_f16 v[54:57], v[168:171], v[18:21], v[14:17]
	v_mfma_f32_16x16x32_f16 v[14:17], v[174:177], v[2:5], v[164:167]
	v_mfma_f32_16x16x32_f16 v[114:117], v[228:231], v[6:9], v[14:17]
	v_mfma_f32_16x16x32_f16 v[14:17], v[174:177], v[10:13], v[86:89]
	v_mfma_f32_16x16x32_f16 v[42:45], v[228:231], v[18:21], v[14:17]
	s_barrier
	s_nop 4
	ds_read_b128 v[14:17], v173 offset:49152
	ds_read_b128 v[22:25], v173 offset:50176
	ds_read_b128 v[30:33], v173 offset:51200
	ds_read_b128 v[34:37], v173 offset:52224
	ds_read_b128 v[46:49], v173 offset:53248
	ds_read_b128 v[58:61], v173 offset:54272
	ds_read_b128 v[70:73], v173 offset:55296
	ds_read_b128 v[86:89], v173 offset:56320
	s_barrier
	s_waitcnt lgkmcnt(0)
	s_waitcnt lgkmcnt(0)
	v_mfma_f32_16x16x32_f16 v[26:29], v[14:17], v[110:113], v[26:29]
	v_mfma_f32_16x16x32_f16 v[174:177], v[22:25], v[130:133], v[26:29]
	v_mfma_f32_16x16x32_f16 v[26:29], v[14:17], v[216:219], v[38:41]
	v_mfma_f32_16x16x32_f16 v[142:145], v[22:25], v[224:227], v[26:29]
	v_mfma_f32_16x16x32_f16 v[26:29], v[30:33], v[110:113], v[50:53]
	v_mfma_f32_16x16x32_f16 v[170:173], v[34:37], v[130:133], v[26:29]
	v_mfma_f32_16x16x32_f16 v[26:29], v[30:33], v[216:219], v[62:65]
	v_mfma_f32_16x16x32_f16 v[138:141], v[34:37], v[224:227], v[26:29]
	v_mfma_f32_16x16x32_f16 v[26:29], v[46:49], v[110:113], v[74:77]
	v_mfma_f32_16x16x32_f16 v[166:169], v[58:61], v[130:133], v[26:29]
	v_mfma_f32_16x16x32_f16 v[26:29], v[46:49], v[216:219], v[82:85]
	v_mfma_f32_16x16x32_f16 v[134:137], v[58:61], v[224:227], v[26:29]
	v_mfma_f32_16x16x32_f16 v[26:29], v[70:73], v[110:113], v[90:93]
	v_mfma_f32_16x16x32_f16 v[162:165], v[86:89], v[130:133], v[26:29]
	v_mfma_f32_16x16x32_f16 v[26:29], v[70:73], v[216:219], v[94:97]
	v_mfma_f32_16x16x32_f16 v[130:133], v[86:89], v[224:227], v[26:29]
	v_mfma_f32_16x16x32_f16 v[26:29], v[14:17], v[2:5], v[98:101]
	v_mfma_f32_16x16x32_f16 v[14:17], v[14:17], v[10:13], v[102:105]
	v_mfma_f32_16x16x32_f16 v[38:41], v[22:25], v[18:21], v[14:17]
	v_mfma_f32_16x16x32_f16 v[14:17], v[30:33], v[2:5], v[106:109]
	v_mfma_f32_16x16x32_f16 v[106:109], v[34:37], v[6:9], v[14:17]
	v_mfma_f32_16x16x32_f16 v[14:17], v[30:33], v[10:13], v[200:203]
	v_mfma_f32_16x16x32_f16 v[110:113], v[22:25], v[6:9], v[26:29]
	v_mfma_f32_16x16x32_f16 v[26:29], v[34:37], v[18:21], v[14:17]
	v_mfma_f32_16x16x32_f16 v[14:17], v[46:49], v[2:5], v[204:207]
	v_mfma_f32_16x16x32_f16 v[2:5], v[70:73], v[2:5], v[212:215]
	v_mfma_f32_16x16x32_f16 v[102:105], v[58:61], v[6:9], v[14:17]
	v_mfma_f32_16x16x32_f16 v[14:17], v[46:49], v[10:13], v[220:223]
	v_mfma_f32_16x16x32_f16 v[98:101], v[86:89], v[6:9], v[2:5]
	v_mfma_f32_16x16x32_f16 v[2:5], v[70:73], v[10:13], v[196:199]
	v_mfma_f32_16x16x32_f16 v[14:17], v[58:61], v[18:21], v[14:17]
	v_mfma_f32_16x16x32_f16 v[2:5], v[86:89], v[18:21], v[2:5]
	s_cmpk_gt_u32 s65, 0xff
	s_barrier
	s_cbranch_scc1 .LBB7_242
	s_barrier

.LBB8_41:
	ds_read_b128 v[182:185], v171
	ds_read_b128 v[186:189], v173
	ds_read_b128 v[190:193], v174
	ds_read_b128 v[194:197], v175
	v_add_u32_e32 v177, 0xc000, v148
	v_lshl_add_u64 v[246:247], v[134:135], 0, s[44:45]
	v_readfirstlane_b32 s47, v177
	v_add_u32_e32 v176, s48, v170
	v_lshl_add_u64 v[178:179], v[246:247], 0, s[28:29]
	s_mov_b32 m0, s47
	ds_read_b128 v[198:201], v176
	ds_read_b128 v[202:205], v176 offset:1024
	ds_read_b128 v[206:209], v176 offset:2048
	ds_read_b128 v[210:213], v176 offset:3072
	ds_read_b128 v[214:217], v176 offset:4096
	ds_read_b128 v[218:221], v176 offset:5120
	ds_read_b128 v[222:225], v176 offset:6144
	ds_read_b128 v[226:229], v176 offset:7168
	global_load_lds_dwordx4 v[178:179], off
	v_add_u32_e32 v178, 0xe000, v148
	v_lshl_add_u64 v[248:249], v[136:137], 0, s[44:45]
	v_readfirstlane_b32 s47, v178
	v_lshl_add_u64 v[230:231], v[248:249], 0, s[28:29]
	s_mov_b32 m0, s47
	s_nop 0
	global_load_lds_dwordx4 v[230:231], off
	s_waitcnt lgkmcnt(8)
	s_barrier
	s_waitcnt lgkmcnt(0)
	s_waitcnt lgkmcnt(0)
	v_mfma_f32_16x16x32_f16 v[126:129], v[198:201], v[182:185], v[126:129]
	v_mfma_f32_16x16x32_f16 v[122:125], v[198:201], v[190:193], v[122:125]
	v_mfma_f32_16x16x32_f16 v[118:121], v[206:209], v[182:185], v[118:121]
	v_mfma_f32_16x16x32_f16 v[114:117], v[206:209], v[190:193], v[114:117]
	v_mfma_f32_16x16x32_f16 v[110:113], v[214:217], v[182:185], v[110:113]
	v_mfma_f32_16x16x32_f16 v[106:109], v[214:217], v[190:193], v[106:109]
	v_mfma_f32_16x16x32_f16 v[102:105], v[222:225], v[182:185], v[102:105]
	v_mfma_f32_16x16x32_f16 v[98:101], v[222:225], v[190:193], v[98:101]
	v_mfma_f32_16x16x32_f16 v[126:129], v[202:205], v[186:189], v[126:129]
	v_mfma_f32_16x16x32_f16 v[122:125], v[202:205], v[194:197], v[122:125]
	v_mfma_f32_16x16x32_f16 v[118:121], v[210:213], v[186:189], v[118:121]
	v_mfma_f32_16x16x32_f16 v[114:117], v[210:213], v[194:197], v[114:117]
	v_mfma_f32_16x16x32_f16 v[110:113], v[218:221], v[186:189], v[110:113]
	v_mfma_f32_16x16x32_f16 v[106:109], v[218:221], v[194:197], v[106:109]
	v_mfma_f32_16x16x32_f16 v[102:105], v[226:229], v[186:189], v[102:105]
	v_mfma_f32_16x16x32_f16 v[98:101], v[226:229], v[194:197], v[98:101]
	s_barrier
	v_lshl_add_u64 v[250:251], v[138:139], 0, s[44:45]
	v_readfirstlane_b32 s47, v142
	v_lshl_add_u64 v[252:253], v[250:251], 0, s[30:31]
	s_mov_b32 m0, s47
	ds_read_b128 v[230:233], v162
	ds_read_b128 v[234:237], v163
	ds_read_b128 v[238:241], v164
	ds_read_b128 v[242:245], v165
	global_load_lds_dwordx4 v[252:253], off
	v_lshl_add_u64 v[252:253], v[140:141], 0, s[44:45]
	v_readfirstlane_b32 s47, v143
	v_lshl_add_u64 v[254:255], v[252:253], 0, s[30:31]
	s_mov_b32 m0, s47
	s_nop 0
	global_load_lds_dwordx4 v[254:255], off
	s_barrier
	s_waitcnt lgkmcnt(0)
	s_waitcnt lgkmcnt(0)
	v_mfma_f32_16x16x32_f16 v[94:97], v[198:201], v[230:233], v[94:97]
	v_mfma_f32_16x16x32_f16 v[90:93], v[198:201], v[238:241], v[90:93]
	v_mfma_f32_16x16x32_f16 v[86:89], v[206:209], v[230:233], v[86:89]
	v_mfma_f32_16x16x32_f16 v[82:85], v[206:209], v[238:241], v[82:85]
	v_mfma_f32_16x16x32_f16 v[78:81], v[214:217], v[230:233], v[78:81]
	v_mfma_f32_16x16x32_f16 v[74:77], v[214:217], v[238:241], v[74:77]
	v_mfma_f32_16x16x32_f16 v[70:73], v[222:225], v[230:233], v[70:73]
	v_mfma_f32_16x16x32_f16 v[66:69], v[222:225], v[238:241], v[66:69]
	v_mfma_f32_16x16x32_f16 v[94:97], v[202:205], v[234:237], v[94:97]
	v_mfma_f32_16x16x32_f16 v[90:93], v[202:205], v[242:245], v[90:93]
	v_mfma_f32_16x16x32_f16 v[86:89], v[210:213], v[234:237], v[86:89]
	v_mfma_f32_16x16x32_f16 v[82:85], v[210:213], v[242:245], v[82:85]
	v_mfma_f32_16x16x32_f16 v[78:81], v[218:221], v[234:237], v[78:81]
	v_mfma_f32_16x16x32_f16 v[74:77], v[218:221], v[242:245], v[74:77]
	v_mfma_f32_16x16x32_f16 v[70:73], v[226:229], v[234:237], v[70:73]
	v_mfma_f32_16x16x32_f16 v[66:69], v[226:229], v[242:245], v[66:69]
	v_readfirstlane_b32 s47, v148
	v_lshl_add_u64 v[254:255], v[246:247], 0, s[30:31]
	s_mov_b32 m0, s47
	v_readfirstlane_b32 s47, v149
	s_barrier
	ds_read_b128 v[198:201], v176 offset:16384
	ds_read_b128 v[202:205], v176 offset:17408
	ds_read_b128 v[206:209], v176 offset:18432
	ds_read_b128 v[210:213], v176 offset:19456
	ds_read_b128 v[214:217], v176 offset:20480
	ds_read_b128 v[218:221], v176 offset:21504
	ds_read_b128 v[222:225], v176 offset:22528
	ds_read_b128 v[226:229], v176 offset:23552
	global_load_lds_dwordx4 v[254:255], off
	v_lshl_add_u64 v[254:255], v[248:249], 0, s[30:31]
	s_mov_b32 m0, s47
	s_nop 0
	global_load_lds_dwordx4 v[254:255], off
	s_barrier
	s_waitcnt lgkmcnt(0)
	s_waitcnt lgkmcnt(0)
	v_mfma_f32_16x16x32_f16 v[62:65], v[198:201], v[182:185], v[62:65]
	v_mfma_f32_16x16x32_f16 v[58:61], v[198:201], v[190:193], v[58:61]
	v_mfma_f32_16x16x32_f16 v[54:57], v[206:209], v[182:185], v[54:57]
	v_mfma_f32_16x16x32_f16 v[50:53], v[206:209], v[190:193], v[50:53]
	v_mfma_f32_16x16x32_f16 v[46:49], v[214:217], v[182:185], v[46:49]
	v_mfma_f32_16x16x32_f16 v[42:45], v[214:217], v[190:193], v[42:45]
	v_mfma_f32_16x16x32_f16 v[38:41], v[222:225], v[182:185], v[38:41]
	v_mfma_f32_16x16x32_f16 v[34:37], v[222:225], v[190:193], v[34:37]
	v_mfma_f32_16x16x32_f16 v[62:65], v[202:205], v[186:189], v[62:65]
	v_mfma_f32_16x16x32_f16 v[58:61], v[202:205], v[194:197], v[58:61]
	v_mfma_f32_16x16x32_f16 v[54:57], v[210:213], v[186:189], v[54:57]
	v_mfma_f32_16x16x32_f16 v[50:53], v[210:213], v[194:197], v[50:53]
	v_mfma_f32_16x16x32_f16 v[46:49], v[218:221], v[186:189], v[46:49]
	v_mfma_f32_16x16x32_f16 v[42:45], v[218:221], v[194:197], v[42:45]
	v_mfma_f32_16x16x32_f16 v[38:41], v[226:229], v[186:189], v[38:41]
	v_mfma_f32_16x16x32_f16 v[34:37], v[226:229], v[194:197], v[34:37]
	s_barrier
	v_readfirstlane_b32 s47, v154
	v_lshl_add_u64 v[182:183], v[250:251], 0, s[34:35]
	s_mov_b32 m0, s47
	v_readfirstlane_b32 s47, v155
	global_load_lds_dwordx4 v[182:183], off
	v_lshl_add_u64 v[182:183], v[252:253], 0, s[34:35]
	s_mov_b32 m0, s47
	s_nop 0
	global_load_lds_dwordx4 v[182:183], off
	s_waitcnt vmcnt(6)
	s_barrier
	v_mfma_f32_16x16x32_f16 v[30:33], v[198:201], v[230:233], v[30:33]
	v_mfma_f32_16x16x32_f16 v[26:29], v[198:201], v[238:241], v[26:29]
	v_mfma_f32_16x16x32_f16 v[22:25], v[206:209], v[230:233], v[22:25]
	v_mfma_f32_16x16x32_f16 v[18:21], v[206:209], v[238:241], v[18:21]
	v_mfma_f32_16x16x32_f16 v[14:17], v[214:217], v[230:233], v[14:17]
	v_mfma_f32_16x16x32_f16 v[10:13], v[214:217], v[238:241], v[10:13]
	v_mfma_f32_16x16x32_f16 v[6:9], v[222:225], v[230:233], v[6:9]
	v_mfma_f32_16x16x32_f16 v[2:5], v[222:225], v[238:241], v[2:5]
	v_mfma_f32_16x16x32_f16 v[30:33], v[202:205], v[234:237], v[30:33]
	v_mfma_f32_16x16x32_f16 v[26:29], v[202:205], v[242:245], v[26:29]
	v_mfma_f32_16x16x32_f16 v[22:25], v[210:213], v[234:237], v[22:25]
	v_mfma_f32_16x16x32_f16 v[18:21], v[210:213], v[242:245], v[18:21]
	v_mfma_f32_16x16x32_f16 v[14:17], v[218:221], v[234:237], v[14:17]
	v_mfma_f32_16x16x32_f16 v[10:13], v[218:221], v[242:245], v[10:13]
	v_mfma_f32_16x16x32_f16 v[6:9], v[226:229], v[234:237], v[6:9]
	v_mfma_f32_16x16x32_f16 v[2:5], v[226:229], v[242:245], v[2:5]
	s_barrier
	ds_read_b128 v[182:185], v144
	ds_read_b128 v[186:189], v145
	ds_read_b128 v[190:193], v146
	ds_read_b128 v[194:197], v147
	v_readfirstlane_b32 s47, v156
	v_lshl_add_u64 v[230:231], v[246:247], 0, s[34:35]
	s_mov_b32 m0, s47
	v_readfirstlane_b32 s47, v157
	ds_read_b128 v[198:201], v176 offset:32768
	ds_read_b128 v[202:205], v176 offset:33792
	ds_read_b128 v[206:209], v176 offset:34816
	ds_read_b128 v[210:213], v176 offset:35840
	ds_read_b128 v[214:217], v176 offset:36864
	ds_read_b128 v[218:221], v176 offset:37888
	ds_read_b128 v[222:225], v176 offset:38912
	ds_read_b128 v[226:229], v176 offset:39936
	global_load_lds_dwordx4 v[230:231], off
	v_lshl_add_u64 v[230:231], v[248:249], 0, s[34:35]
	s_mov_b32 m0, s47
	s_nop 0
	global_load_lds_dwordx4 v[230:231], off
	s_waitcnt lgkmcnt(8)
	s_barrier
	s_waitcnt lgkmcnt(0)
	s_waitcnt lgkmcnt(0)
	v_mfma_f32_16x16x32_f16 v[126:129], v[198:201], v[182:185], v[126:129]
	v_mfma_f32_16x16x32_f16 v[122:125], v[198:201], v[190:193], v[122:125]
	v_mfma_f32_16x16x32_f16 v[118:121], v[206:209], v[182:185], v[118:121]
	v_mfma_f32_16x16x32_f16 v[114:117], v[206:209], v[190:193], v[114:117]
	v_mfma_f32_16x16x32_f16 v[110:113], v[214:217], v[182:185], v[110:113]
	v_mfma_f32_16x16x32_f16 v[106:109], v[214:217], v[190:193], v[106:109]
	v_mfma_f32_16x16x32_f16 v[102:105], v[222:225], v[182:185], v[102:105]
	v_mfma_f32_16x16x32_f16 v[98:101], v[222:225], v[190:193], v[98:101]
	v_mfma_f32_16x16x32_f16 v[126:129], v[202:205], v[186:189], v[126:129]
	v_mfma_f32_16x16x32_f16 v[122:125], v[202:205], v[194:197], v[122:125]
	v_mfma_f32_16x16x32_f16 v[118:121], v[210:213], v[186:189], v[118:121]
	v_mfma_f32_16x16x32_f16 v[114:117], v[210:213], v[194:197], v[114:117]
	v_mfma_f32_16x16x32_f16 v[110:113], v[218:221], v[186:189], v[110:113]
	v_mfma_f32_16x16x32_f16 v[106:109], v[218:221], v[194:197], v[106:109]
	v_mfma_f32_16x16x32_f16 v[102:105], v[226:229], v[186:189], v[102:105]
	v_mfma_f32_16x16x32_f16 v[98:101], v[226:229], v[194:197], v[98:101]
	s_barrier
	v_readfirstlane_b32 s47, v158
	v_lshl_add_u64 v[254:255], v[250:251], 0, s[36:37]
	s_mov_b32 m0, s47
	v_readfirstlane_b32 s47, v160
	ds_read_b128 v[230:233], v150
	ds_read_b128 v[234:237], v151
	ds_read_b128 v[238:241], v152
	ds_read_b128 v[242:245], v153
	global_load_lds_dwordx4 v[254:255], off
	v_lshl_add_u64 v[254:255], v[252:253], 0, s[36:37]
	s_mov_b32 m0, s47
	s_nop 0
	global_load_lds_dwordx4 v[254:255], off
	s_barrier
	s_waitcnt lgkmcnt(0)
	s_waitcnt lgkmcnt(0)
	v_mfma_f32_16x16x32_f16 v[94:97], v[198:201], v[230:233], v[94:97]
	v_mfma_f32_16x16x32_f16 v[90:93], v[198:201], v[238:241], v[90:93]
	v_mfma_f32_16x16x32_f16 v[86:89], v[206:209], v[230:233], v[86:89]
	v_mfma_f32_16x16x32_f16 v[82:85], v[206:209], v[238:241], v[82:85]
	v_mfma_f32_16x16x32_f16 v[78:81], v[214:217], v[230:233], v[78:81]
	v_mfma_f32_16x16x32_f16 v[74:77], v[214:217], v[238:241], v[74:77]
	v_mfma_f32_16x16x32_f16 v[70:73], v[222:225], v[230:233], v[70:73]
	v_mfma_f32_16x16x32_f16 v[66:69], v[222:225], v[238:241], v[66:69]
	v_mfma_f32_16x16x32_f16 v[94:97], v[202:205], v[234:237], v[94:97]
	v_mfma_f32_16x16x32_f16 v[90:93], v[202:205], v[242:245], v[90:93]
	v_mfma_f32_16x16x32_f16 v[86:89], v[210:213], v[234:237], v[86:89]
	v_mfma_f32_16x16x32_f16 v[82:85], v[210:213], v[242:245], v[82:85]
	v_mfma_f32_16x16x32_f16 v[78:81], v[218:221], v[234:237], v[78:81]
	v_mfma_f32_16x16x32_f16 v[74:77], v[218:221], v[242:245], v[74:77]
	v_mfma_f32_16x16x32_f16 v[70:73], v[226:229], v[234:237], v[70:73]
	v_mfma_f32_16x16x32_f16 v[66:69], v[226:229], v[242:245], v[66:69]
	v_readfirstlane_b32 s47, v161
	v_lshl_add_u64 v[246:247], v[246:247], 0, s[36:37]
	s_mov_b32 m0, s47
	v_readfirstlane_b32 s47, v166
	s_barrier
	ds_read_b128 v[198:201], v176 offset:49152
	ds_read_b128 v[202:205], v176 offset:50176
	ds_read_b128 v[206:209], v176 offset:51200
	ds_read_b128 v[210:213], v176 offset:52224
	ds_read_b128 v[214:217], v176 offset:53248
	ds_read_b128 v[218:221], v176 offset:54272
	ds_read_b128 v[222:225], v176 offset:55296
	ds_read_b128 v[226:229], v176 offset:56320
	global_load_lds_dwordx4 v[246:247], off
	v_lshl_add_u64 v[246:247], v[248:249], 0, s[36:37]
	s_mov_b32 m0, s47
	s_nop 0
	global_load_lds_dwordx4 v[246:247], off
	s_barrier
	s_waitcnt lgkmcnt(0)
	s_waitcnt lgkmcnt(0)
	v_mfma_f32_16x16x32_f16 v[62:65], v[198:201], v[182:185], v[62:65]
	v_mfma_f32_16x16x32_f16 v[58:61], v[198:201], v[190:193], v[58:61]
	v_mfma_f32_16x16x32_f16 v[54:57], v[206:209], v[182:185], v[54:57]
	v_mfma_f32_16x16x32_f16 v[50:53], v[206:209], v[190:193], v[50:53]
	v_mfma_f32_16x16x32_f16 v[46:49], v[214:217], v[182:185], v[46:49]
	v_mfma_f32_16x16x32_f16 v[42:45], v[214:217], v[190:193], v[42:45]
	v_mfma_f32_16x16x32_f16 v[38:41], v[222:225], v[182:185], v[38:41]
	v_mfma_f32_16x16x32_f16 v[34:37], v[222:225], v[190:193], v[34:37]
	v_mfma_f32_16x16x32_f16 v[62:65], v[202:205], v[186:189], v[62:65]
	v_mfma_f32_16x16x32_f16 v[58:61], v[202:205], v[194:197], v[58:61]
	v_mfma_f32_16x16x32_f16 v[54:57], v[210:213], v[186:189], v[54:57]
	v_mfma_f32_16x16x32_f16 v[50:53], v[210:213], v[194:197], v[50:53]
	v_mfma_f32_16x16x32_f16 v[46:49], v[218:221], v[186:189], v[46:49]
	v_mfma_f32_16x16x32_f16 v[42:45], v[218:221], v[194:197], v[42:45]
	v_mfma_f32_16x16x32_f16 v[38:41], v[226:229], v[186:189], v[38:41]
	v_mfma_f32_16x16x32_f16 v[34:37], v[226:229], v[194:197], v[34:37]
	s_barrier
	v_readfirstlane_b32 s47, v168
	v_lshl_add_u64 v[182:183], v[250:251], 0, s[38:39]
	s_mov_b32 m0, s47
	v_readfirstlane_b32 s47, v169
	global_load_lds_dwordx4 v[182:183], off
	v_lshl_add_u64 v[182:183], v[252:253], 0, s[38:39]
	s_mov_b32 m0, s47
	s_nop 0
	global_load_lds_dwordx4 v[182:183], off
	s_waitcnt vmcnt(6)
	s_barrier
	v_mfma_f32_16x16x32_f16 v[30:33], v[198:201], v[230:233], v[30:33]
	v_mfma_f32_16x16x32_f16 v[26:29], v[198:201], v[238:241], v[26:29]
	v_mfma_f32_16x16x32_f16 v[22:25], v[206:209], v[230:233], v[22:25]
	v_mfma_f32_16x16x32_f16 v[18:21], v[206:209], v[238:241], v[18:21]
	v_mfma_f32_16x16x32_f16 v[14:17], v[214:217], v[230:233], v[14:17]
	v_mfma_f32_16x16x32_f16 v[10:13], v[214:217], v[238:241], v[10:13]
	v_mfma_f32_16x16x32_f16 v[6:9], v[222:225], v[230:233], v[6:9]
	v_mfma_f32_16x16x32_f16 v[2:5], v[222:225], v[238:241], v[2:5]
	v_mfma_f32_16x16x32_f16 v[30:33], v[202:205], v[234:237], v[30:33]
	v_mfma_f32_16x16x32_f16 v[26:29], v[202:205], v[242:245], v[26:29]
	v_mfma_f32_16x16x32_f16 v[22:25], v[210:213], v[234:237], v[22:25]
	v_mfma_f32_16x16x32_f16 v[18:21], v[210:213], v[242:245], v[18:21]
	v_mfma_f32_16x16x32_f16 v[14:17], v[218:221], v[234:237], v[14:17]
	v_mfma_f32_16x16x32_f16 v[10:13], v[218:221], v[242:245], v[10:13]
	v_mfma_f32_16x16x32_f16 v[6:9], v[226:229], v[234:237], v[6:9]
	v_mfma_f32_16x16x32_f16 v[2:5], v[226:229], v[242:245], v[2:5]
	s_add_i32 s46, s46, 2
	s_add_u32 s44, s44, 0x100
	s_addc_u32 s45, s45, 0
	s_cmp_lt_u32 s46, 4
	s_barrier
	s_cbranch_scc1 .LBB8_41
	s_add_u32 s42, s42, 0x20380
	s_addc_u32 s43, s43, 0
	v_readfirstlane_b32 s44, v177
	v_lshl_add_u64 v[130:131], v[130:131], 1, s[42:43]
	s_mov_b32 m0, s44
	ds_read_b128 v[134:137], v171
	ds_read_b128 v[138:141], v173
	ds_read_b128 v[154:157], v174
	ds_read_b128 v[168:171], v175
	ds_read_b128 v[182:185], v176
	ds_read_b128 v[186:189], v176 offset:1024
	ds_read_b128 v[190:193], v176 offset:2048
	ds_read_b128 v[194:197], v176 offset:3072
	ds_read_b128 v[198:201], v176 offset:4096
	ds_read_b128 v[202:205], v176 offset:5120
	ds_read_b128 v[206:209], v176 offset:6144
	ds_read_b128 v[210:213], v176 offset:7168
	global_load_lds_dwordx4 v[130:131], off
	v_lshl_add_u64 v[130:131], v[132:133], 1, s[42:43]
	v_readfirstlane_b32 s42, v178
	s_mov_b32 m0, s42
	s_nop 0
	global_load_lds_dwordx4 v[130:131], off
	s_barrier
	s_waitcnt lgkmcnt(0)
	s_waitcnt lgkmcnt(0)
	v_mfma_f32_16x16x32_f16 v[122:125], v[182:185], v[154:157], v[122:125]
	v_mfma_f32_16x16x32_f16 v[110:113], v[198:201], v[134:137], v[110:113]
	v_mfma_f32_16x16x32_f16 v[98:101], v[206:209], v[154:157], v[98:101]
	v_mfma_f32_16x16x32_f16 v[126:129], v[182:185], v[134:137], v[126:129]
	v_mfma_f32_16x16x32_f16 v[122:125], v[186:189], v[168:171], v[122:125]
	v_mfma_f32_16x16x32_f16 v[118:121], v[190:193], v[134:137], v[118:121]
	v_mfma_f32_16x16x32_f16 v[114:117], v[190:193], v[154:157], v[114:117]
	v_mfma_f32_16x16x32_f16 v[130:133], v[202:205], v[138:141], v[110:113]
	v_mfma_f32_16x16x32_f16 v[106:109], v[198:201], v[154:157], v[106:109]
	v_mfma_f32_16x16x32_f16 v[102:105], v[206:209], v[134:137], v[102:105]
	v_mfma_f32_16x16x32_f16 v[98:101], v[210:213], v[168:171], v[98:101]
	v_mfma_f32_16x16x32_f16 v[126:129], v[186:189], v[138:141], v[126:129]
	v_mfma_f32_16x16x32_f16 v[118:121], v[194:197], v[138:141], v[118:121]
	v_mfma_f32_16x16x32_f16 v[114:117], v[194:197], v[168:171], v[114:117]
	v_mfma_f32_16x16x32_f16 v[214:217], v[202:205], v[168:171], v[106:109]
	v_mfma_f32_16x16x32_f16 v[102:105], v[210:213], v[138:141], v[102:105]
	s_barrier
	ds_read_b128 v[106:109], v162
	ds_read_b128 v[110:113], v163
	ds_read_b128 v[160:163], v164
	ds_read_b128 v[218:221], v165
	s_barrier
	s_waitcnt lgkmcnt(0)
	s_waitcnt lgkmcnt(0)
	v_mfma_f32_16x16x32_f16 v[82:85], v[190:193], v[160:163], v[82:85]
	v_mfma_f32_16x16x32_f16 v[78:81], v[198:201], v[106:109], v[78:81]
	v_mfma_f32_16x16x32_f16 v[74:77], v[198:201], v[160:163], v[74:77]
	v_mfma_f32_16x16x32_f16 v[70:73], v[206:209], v[106:109], v[70:73]
	v_mfma_f32_16x16x32_f16 v[66:69], v[206:209], v[160:163], v[66:69]
	v_mfma_f32_16x16x32_f16 v[94:97], v[182:185], v[106:109], v[94:97]
	v_mfma_f32_16x16x32_f16 v[90:93], v[182:185], v[160:163], v[90:93]
	v_mfma_f32_16x16x32_f16 v[86:89], v[190:193], v[106:109], v[86:89]
	v_mfma_f32_16x16x32_f16 v[82:85], v[194:197], v[218:221], v[82:85]
	v_mfma_f32_16x16x32_f16 v[78:81], v[202:205], v[110:113], v[78:81]
	v_mfma_f32_16x16x32_f16 v[74:77], v[202:205], v[218:221], v[74:77]
	v_mfma_f32_16x16x32_f16 v[70:73], v[210:213], v[110:113], v[70:73]
	v_mfma_f32_16x16x32_f16 v[66:69], v[210:213], v[218:221], v[66:69]
	v_mfma_f32_16x16x32_f16 v[222:225], v[186:189], v[110:113], v[94:97]
	v_mfma_f32_16x16x32_f16 v[182:185], v[186:189], v[218:221], v[90:93]
	v_mfma_f32_16x16x32_f16 v[86:89], v[194:197], v[110:113], v[86:89]
	s_barrier
	ds_read_b128 v[90:93], v176 offset:16384
	ds_read_b128 v[94:97], v176 offset:17408
	ds_read_b128 v[186:189], v176 offset:18432
	ds_read_b128 v[190:193], v176 offset:19456
	ds_read_b128 v[194:197], v176 offset:20480
	ds_read_b128 v[198:201], v176 offset:21504
	ds_read_b128 v[202:205], v176 offset:22528
	ds_read_b128 v[206:209], v176 offset:23552
	s_waitcnt vmcnt(4)
	s_barrier
	s_waitcnt lgkmcnt(0)
	s_waitcnt lgkmcnt(0)
	v_mfma_f32_16x16x32_f16 v[46:49], v[194:197], v[134:137], v[46:49]
	v_mfma_f32_16x16x32_f16 v[42:45], v[194:197], v[154:157], v[42:45]
	v_mfma_f32_16x16x32_f16 v[38:41], v[202:205], v[134:137], v[38:41]
	v_mfma_f32_16x16x32_f16 v[34:37], v[202:205], v[154:157], v[34:37]
	v_mfma_f32_16x16x32_f16 v[62:65], v[90:93], v[134:137], v[62:65]
	v_mfma_f32_16x16x32_f16 v[58:61], v[90:93], v[154:157], v[58:61]
	v_mfma_f32_16x16x32_f16 v[54:57], v[186:189], v[134:137], v[54:57]
	v_mfma_f32_16x16x32_f16 v[50:53], v[186:189], v[154:157], v[50:53]
	v_mfma_f32_16x16x32_f16 v[46:49], v[198:201], v[138:141], v[46:49]
	v_mfma_f32_16x16x32_f16 v[42:45], v[198:201], v[168:171], v[42:45]
	v_mfma_f32_16x16x32_f16 v[38:41], v[206:209], v[138:141], v[38:41]
	v_mfma_f32_16x16x32_f16 v[34:37], v[206:209], v[168:171], v[34:37]
	v_mfma_f32_16x16x32_f16 v[210:213], v[94:97], v[138:141], v[62:65]
	v_mfma_f32_16x16x32_f16 v[226:229], v[94:97], v[168:171], v[58:61]
	v_mfma_f32_16x16x32_f16 v[230:233], v[190:193], v[138:141], v[54:57]
	v_mfma_f32_16x16x32_f16 v[234:237], v[190:193], v[168:171], v[50:53]
	v_mfma_f32_16x16x32_f16 v[2:5], v[202:205], v[160:163], v[2:5]
	v_mfma_f32_16x16x32_f16 v[30:33], v[90:93], v[106:109], v[30:33]
	v_mfma_f32_16x16x32_f16 v[26:29], v[90:93], v[160:163], v[26:29]
	v_mfma_f32_16x16x32_f16 v[22:25], v[186:189], v[106:109], v[22:25]
	v_mfma_f32_16x16x32_f16 v[18:21], v[186:189], v[160:163], v[18:21]
	v_mfma_f32_16x16x32_f16 v[14:17], v[194:197], v[106:109], v[14:17]
	v_mfma_f32_16x16x32_f16 v[10:13], v[194:197], v[160:163], v[10:13]
	v_mfma_f32_16x16x32_f16 v[6:9], v[202:205], v[106:109], v[6:9]
	v_mfma_f32_16x16x32_f16 v[2:5], v[206:209], v[218:221], v[2:5]
	v_mfma_f32_16x16x32_f16 v[138:141], v[94:97], v[110:113], v[30:33]
	v_mfma_f32_16x16x32_f16 v[168:171], v[94:97], v[218:221], v[26:29]
	v_mfma_f32_16x16x32_f16 v[238:241], v[190:193], v[110:113], v[22:25]
	v_mfma_f32_16x16x32_f16 v[186:189], v[190:193], v[218:221], v[18:21]
	v_mfma_f32_16x16x32_f16 v[190:193], v[198:201], v[110:113], v[14:17]
	v_mfma_f32_16x16x32_f16 v[194:197], v[198:201], v[218:221], v[10:13]
	v_mfma_f32_16x16x32_f16 v[198:201], v[206:209], v[110:113], v[6:9]
	s_barrier
	s_nop 0
	ds_read_b128 v[6:9], v144
	ds_read_b128 v[10:13], v145
	ds_read_b128 v[14:17], v146
	ds_read_b128 v[160:163], v147
	ds_read_b128 v[18:21], v176 offset:32768
	ds_read_b128 v[22:25], v176 offset:33792
	ds_read_b128 v[26:29], v176 offset:34816
	ds_read_b128 v[50:53], v176 offset:35840
	ds_read_b128 v[202:205], v176 offset:36864
	ds_read_b128 v[206:209], v176 offset:37888
	ds_read_b128 v[218:221], v176 offset:38912
	ds_read_b128 v[242:245], v176 offset:39936
	s_waitcnt vmcnt(2)
	s_barrier
	s_waitcnt lgkmcnt(0)
	s_waitcnt lgkmcnt(0)
	v_mfma_f32_16x16x32_f16 v[30:33], v[18:21], v[6:9], v[126:129]
	v_mfma_f32_16x16x32_f16 v[154:157], v[22:25], v[10:13], v[30:33]
	v_mfma_f32_16x16x32_f16 v[30:33], v[18:21], v[14:17], v[122:125]
	v_mfma_f32_16x16x32_f16 v[110:113], v[22:25], v[160:163], v[30:33]
	v_mfma_f32_16x16x32_f16 v[30:33], v[26:29], v[6:9], v[118:121]
	v_mfma_f32_16x16x32_f16 v[146:149], v[50:53], v[10:13], v[30:33]
	v_mfma_f32_16x16x32_f16 v[30:33], v[26:29], v[14:17], v[114:117]
	v_mfma_f32_16x16x32_f16 v[106:109], v[50:53], v[160:163], v[30:33]
	v_mfma_f32_16x16x32_f16 v[30:33], v[202:205], v[6:9], v[130:133]
	v_mfma_f32_16x16x32_f16 v[142:145], v[206:209], v[10:13], v[30:33]
	v_mfma_f32_16x16x32_f16 v[30:33], v[202:205], v[14:17], v[214:217]
	v_mfma_f32_16x16x32_f16 v[94:97], v[206:209], v[160:163], v[30:33]
	v_mfma_f32_16x16x32_f16 v[30:33], v[218:221], v[6:9], v[102:105]
	v_mfma_f32_16x16x32_f16 v[134:137], v[242:245], v[10:13], v[30:33]
	v_mfma_f32_16x16x32_f16 v[30:33], v[218:221], v[14:17], v[98:101]
	v_mfma_f32_16x16x32_f16 v[90:93], v[242:245], v[160:163], v[30:33]
	s_barrier
	ds_read_b128 v[102:105], v150
	ds_read_b128 v[114:117], v151
	ds_read_b128 v[118:121], v152
	ds_read_b128 v[126:129], v153
	s_waitcnt vmcnt(0)
	s_barrier
	s_waitcnt lgkmcnt(0)
	s_waitcnt lgkmcnt(0)
	v_mfma_f32_16x16x32_f16 v[30:33], v[18:21], v[102:105], v[222:225]
	v_mfma_f32_16x16x32_f16 v[18:21], v[18:21], v[118:121], v[182:185]
	v_mfma_f32_16x16x32_f16 v[62:65], v[22:25], v[114:117], v[30:33]
	v_mfma_f32_16x16x32_f16 v[30:33], v[22:25], v[126:129], v[18:21]
	v_mfma_f32_16x16x32_f16 v[18:21], v[26:29], v[102:105], v[86:89]
	v_mfma_f32_16x16x32_f16 v[58:61], v[50:53], v[114:117], v[18:21]
	v_mfma_f32_16x16x32_f16 v[18:21], v[26:29], v[118:121], v[82:85]
	v_mfma_f32_16x16x32_f16 v[26:29], v[50:53], v[126:129], v[18:21]
	v_mfma_f32_16x16x32_f16 v[18:21], v[202:205], v[102:105], v[78:81]
	v_mfma_f32_16x16x32_f16 v[54:57], v[206:209], v[114:117], v[18:21]
	v_mfma_f32_16x16x32_f16 v[18:21], v[202:205], v[118:121], v[74:77]
	v_mfma_f32_16x16x32_f16 v[22:25], v[206:209], v[126:129], v[18:21]
	v_mfma_f32_16x16x32_f16 v[18:21], v[218:221], v[102:105], v[70:73]
	v_mfma_f32_16x16x32_f16 v[50:53], v[242:245], v[114:117], v[18:21]
	v_mfma_f32_16x16x32_f16 v[18:21], v[218:221], v[118:121], v[66:69]
	v_mfma_f32_16x16x32_f16 v[18:21], v[242:245], v[126:129], v[18:21]
	s_barrier
	ds_read_b128 v[86:89], v176 offset:49152
	ds_read_b128 v[150:153], v176 offset:50176
	ds_read_b128 v[182:185], v176 offset:51200
	ds_read_b128 v[202:205], v176 offset:52224
	ds_read_b128 v[206:209], v176 offset:53248
	ds_read_b128 v[214:217], v176 offset:54272
	ds_read_b128 v[218:221], v176 offset:55296
	ds_read_b128 v[174:177], v176 offset:56320
	s_barrier
	s_waitcnt lgkmcnt(0)
	s_waitcnt lgkmcnt(0)
	v_mfma_f32_16x16x32_f16 v[66:69], v[86:89], v[6:9], v[210:213]
	v_mfma_f32_16x16x32_f16 v[130:133], v[150:153], v[10:13], v[66:69]
	v_mfma_f32_16x16x32_f16 v[66:69], v[86:89], v[14:17], v[226:229]
	v_mfma_f32_16x16x32_f16 v[78:81], v[150:153], v[160:163], v[66:69]
	v_mfma_f32_16x16x32_f16 v[66:69], v[182:185], v[6:9], v[230:233]
	v_mfma_f32_16x16x32_f16 v[46:49], v[206:209], v[6:9], v[46:49]
	v_mfma_f32_16x16x32_f16 v[6:9], v[218:221], v[6:9], v[38:41]
	v_mfma_f32_16x16x32_f16 v[122:125], v[202:205], v[10:13], v[66:69]
	v_mfma_f32_16x16x32_f16 v[66:69], v[182:185], v[14:17], v[234:237]
	v_mfma_f32_16x16x32_f16 v[42:45], v[206:209], v[14:17], v[42:45]
	v_mfma_f32_16x16x32_f16 v[82:85], v[174:177], v[10:13], v[6:9]
	v_mfma_f32_16x16x32_f16 v[6:9], v[218:221], v[14:17], v[34:37]
	v_mfma_f32_16x16x32_f16 v[74:77], v[202:205], v[160:163], v[66:69]
	v_mfma_f32_16x16x32_f16 v[98:101], v[214:217], v[10:13], v[46:49]
	v_mfma_f32_16x16x32_f16 v[70:73], v[214:217], v[160:163], v[42:45]
	v_mfma_f32_16x16x32_f16 v[66:69], v[174:177], v[160:163], v[6:9]
	v_mfma_f32_16x16x32_f16 v[6:9], v[86:89], v[102:105], v[138:141]
	v_mfma_f32_16x16x32_f16 v[46:49], v[150:153], v[114:117], v[6:9]
	v_mfma_f32_16x16x32_f16 v[6:9], v[86:89], v[118:121], v[168:171]
	v_mfma_f32_16x16x32_f16 v[14:17], v[150:153], v[126:129], v[6:9]
	v_mfma_f32_16x16x32_f16 v[6:9], v[182:185], v[102:105], v[238:241]
	v_mfma_f32_16x16x32_f16 v[42:45], v[202:205], v[114:117], v[6:9]
	v_mfma_f32_16x16x32_f16 v[6:9], v[182:185], v[118:121], v[186:189]
	v_mfma_f32_16x16x32_f16 v[10:13], v[202:205], v[126:129], v[6:9]
	v_mfma_f32_16x16x32_f16 v[6:9], v[206:209], v[102:105], v[190:193]
	v_mfma_f32_16x16x32_f16 v[38:41], v[214:217], v[114:117], v[6:9]
	v_mfma_f32_16x16x32_f16 v[6:9], v[206:209], v[118:121], v[194:197]
	v_mfma_f32_16x16x32_f16 v[34:37], v[218:221], v[102:105], v[198:201]
	v_mfma_f32_16x16x32_f16 v[2:5], v[218:221], v[118:121], v[2:5]
	v_mfma_f32_16x16x32_f16 v[6:9], v[214:217], v[126:129], v[6:9]
	v_mfma_f32_16x16x32_f16 v[34:37], v[174:177], v[114:117], v[34:37]
	v_mfma_f32_16x16x32_f16 v[2:5], v[174:177], v[126:129], v[2:5]
	s_cmpk_gt_u32 s62, 0xff
	s_barrier
	s_cbranch_scc1 .LBB8_44
	s_barrier

.LBB9_38:
	ds_read_b128 v[176:179], v169
	ds_read_b128 v[180:183], v170
	ds_read_b128 v[184:187], v171
	ds_read_b128 v[188:191], v172
	v_add_u32_e32 v174, 0xc000, v152
	v_lshl_add_u64 v[192:193], v[136:137], 0, s[42:43]
	v_readfirstlane_b32 s45, v174
	v_add_u32_e32 v175, 0xe000, v152
	v_add_u32_e32 v173, s39, v168
	v_lshl_add_u64 v[230:231], v[192:193], 0, s[10:11]
	s_mov_b32 m0, s45
	v_lshl_add_u64 v[246:247], v[134:135], 0, s[42:43]
	v_readfirstlane_b32 s45, v175
	ds_read_b128 v[198:201], v173
	ds_read_b128 v[202:205], v173 offset:1024
	ds_read_b128 v[206:209], v173 offset:2048
	ds_read_b128 v[210:213], v173 offset:3072
	ds_read_b128 v[214:217], v173 offset:4096
	ds_read_b128 v[218:221], v173 offset:5120
	ds_read_b128 v[222:225], v173 offset:6144
	ds_read_b128 v[226:229], v173 offset:7168
	global_load_lds_dwordx4 v[230:231], off
	v_lshl_add_u64 v[230:231], v[246:247], 0, s[10:11]
	s_mov_b32 m0, s45
	s_nop 0
	global_load_lds_dwordx4 v[230:231], off
	s_waitcnt lgkmcnt(8)
	s_barrier
	s_waitcnt lgkmcnt(0)
	s_waitcnt lgkmcnt(0)
	v_mfma_f32_16x16x32_f16 v[2:5], v[198:201], v[176:179], v[2:5]
	v_mfma_f32_16x16x32_f16 v[6:9], v[198:201], v[184:187], v[6:9]
	v_mfma_f32_16x16x32_f16 v[10:13], v[206:209], v[176:179], v[10:13]
	v_mfma_f32_16x16x32_f16 v[18:21], v[206:209], v[184:187], v[18:21]
	v_mfma_f32_16x16x32_f16 v[30:33], v[214:217], v[176:179], v[30:33]
	v_mfma_f32_16x16x32_f16 v[42:45], v[214:217], v[184:187], v[42:45]
	v_mfma_f32_16x16x32_f16 v[54:57], v[222:225], v[176:179], v[54:57]
	v_mfma_f32_16x16x32_f16 v[66:69], v[222:225], v[184:187], v[66:69]
	v_mfma_f32_16x16x32_f16 v[2:5], v[202:205], v[180:183], v[2:5]
	v_mfma_f32_16x16x32_f16 v[6:9], v[202:205], v[188:191], v[6:9]
	v_mfma_f32_16x16x32_f16 v[10:13], v[210:213], v[180:183], v[10:13]
	v_mfma_f32_16x16x32_f16 v[18:21], v[210:213], v[188:191], v[18:21]
	v_mfma_f32_16x16x32_f16 v[30:33], v[218:221], v[180:183], v[30:33]
	v_mfma_f32_16x16x32_f16 v[42:45], v[218:221], v[188:191], v[42:45]
	v_mfma_f32_16x16x32_f16 v[54:57], v[226:229], v[180:183], v[54:57]
	v_mfma_f32_16x16x32_f16 v[66:69], v[226:229], v[188:191], v[66:69]
	s_barrier
	v_lshl_add_u64 v[248:249], v[140:141], 0, s[42:43]
	v_readfirstlane_b32 s45, v142
	v_lshl_add_u64 v[250:251], v[248:249], 0, s[26:27]
	s_mov_b32 m0, s45
	ds_read_b128 v[230:233], v161
	ds_read_b128 v[234:237], v162
	ds_read_b128 v[238:241], v163
	ds_read_b128 v[242:245], v164
	global_load_lds_dwordx4 v[250:251], off
	v_lshl_add_u64 v[250:251], v[138:139], 0, s[42:43]
	v_readfirstlane_b32 s45, v143
	v_lshl_add_u64 v[252:253], v[250:251], 0, s[26:27]
	s_mov_b32 m0, s45
	s_nop 0
	global_load_lds_dwordx4 v[252:253], off
	s_barrier
	s_waitcnt lgkmcnt(0)
	s_waitcnt lgkmcnt(0)
	v_mfma_f32_16x16x32_f16 v[14:17], v[198:201], v[230:233], v[14:17]
	v_mfma_f32_16x16x32_f16 v[22:25], v[198:201], v[238:241], v[22:25]
	v_mfma_f32_16x16x32_f16 v[34:37], v[206:209], v[230:233], v[34:37]
	v_mfma_f32_16x16x32_f16 v[46:49], v[206:209], v[238:241], v[46:49]
	v_mfma_f32_16x16x32_f16 v[58:61], v[214:217], v[230:233], v[58:61]
	v_mfma_f32_16x16x32_f16 v[70:73], v[214:217], v[238:241], v[70:73]
	v_mfma_f32_16x16x32_f16 v[78:81], v[222:225], v[230:233], v[78:81]
	v_mfma_f32_16x16x32_f16 v[86:89], v[222:225], v[238:241], v[86:89]
	v_mfma_f32_16x16x32_f16 v[14:17], v[202:205], v[234:237], v[14:17]
	v_mfma_f32_16x16x32_f16 v[22:25], v[202:205], v[242:245], v[22:25]
	v_mfma_f32_16x16x32_f16 v[34:37], v[210:213], v[234:237], v[34:37]
	v_mfma_f32_16x16x32_f16 v[46:49], v[210:213], v[242:245], v[46:49]
	v_mfma_f32_16x16x32_f16 v[58:61], v[218:221], v[234:237], v[58:61]
	v_mfma_f32_16x16x32_f16 v[70:73], v[218:221], v[242:245], v[70:73]
	v_mfma_f32_16x16x32_f16 v[78:81], v[226:229], v[234:237], v[78:81]
	v_mfma_f32_16x16x32_f16 v[86:89], v[226:229], v[242:245], v[86:89]
	v_readfirstlane_b32 s45, v152
	v_lshl_add_u64 v[252:253], v[192:193], 0, s[26:27]
	s_mov_b32 m0, s45
	v_readfirstlane_b32 s45, v153
	s_barrier
	ds_read_b128 v[198:201], v173 offset:16384
	ds_read_b128 v[202:205], v173 offset:17408
	ds_read_b128 v[206:209], v173 offset:18432
	ds_read_b128 v[210:213], v173 offset:19456
	ds_read_b128 v[214:217], v173 offset:20480
	ds_read_b128 v[218:221], v173 offset:21504
	ds_read_b128 v[222:225], v173 offset:22528
	ds_read_b128 v[226:229], v173 offset:23552
	global_load_lds_dwordx4 v[252:253], off
	v_lshl_add_u64 v[252:253], v[246:247], 0, s[26:27]
	s_mov_b32 m0, s45
	s_nop 0
	global_load_lds_dwordx4 v[252:253], off
	s_barrier
	s_waitcnt lgkmcnt(0)
	s_waitcnt lgkmcnt(0)
	v_mfma_f32_16x16x32_f16 v[26:29], v[198:201], v[176:179], v[26:29]
	v_mfma_f32_16x16x32_f16 v[38:41], v[198:201], v[184:187], v[38:41]
	v_mfma_f32_16x16x32_f16 v[50:53], v[206:209], v[176:179], v[50:53]
	v_mfma_f32_16x16x32_f16 v[62:65], v[206:209], v[184:187], v[62:65]
	v_mfma_f32_16x16x32_f16 v[74:77], v[214:217], v[176:179], v[74:77]
	v_mfma_f32_16x16x32_f16 v[82:85], v[214:217], v[184:187], v[82:85]
	v_mfma_f32_16x16x32_f16 v[90:93], v[222:225], v[176:179], v[90:93]
	v_mfma_f32_16x16x32_f16 v[94:97], v[222:225], v[184:187], v[94:97]
	v_mfma_f32_16x16x32_f16 v[26:29], v[202:205], v[180:183], v[26:29]
	v_mfma_f32_16x16x32_f16 v[38:41], v[202:205], v[188:191], v[38:41]
	v_mfma_f32_16x16x32_f16 v[50:53], v[210:213], v[180:183], v[50:53]
	v_mfma_f32_16x16x32_f16 v[62:65], v[210:213], v[188:191], v[62:65]
	v_mfma_f32_16x16x32_f16 v[74:77], v[218:221], v[180:183], v[74:77]
	v_mfma_f32_16x16x32_f16 v[82:85], v[218:221], v[188:191], v[82:85]
	v_mfma_f32_16x16x32_f16 v[90:93], v[226:229], v[180:183], v[90:93]
	v_mfma_f32_16x16x32_f16 v[94:97], v[226:229], v[188:191], v[94:97]
	s_barrier
	v_readfirstlane_b32 s45, v154
	v_lshl_add_u64 v[176:177], v[248:249], 0, s[28:29]
	s_mov_b32 m0, s45
	v_readfirstlane_b32 s45, v155
	global_load_lds_dwordx4 v[176:177], off
	v_lshl_add_u64 v[176:177], v[250:251], 0, s[28:29]
	s_mov_b32 m0, s45
	s_nop 0
	global_load_lds_dwordx4 v[176:177], off
	s_waitcnt vmcnt(6)
	s_barrier
	v_mfma_f32_16x16x32_f16 v[98:101], v[198:201], v[230:233], v[98:101]
	v_mfma_f32_16x16x32_f16 v[102:105], v[198:201], v[238:241], v[102:105]
	v_mfma_f32_16x16x32_f16 v[106:109], v[206:209], v[230:233], v[106:109]
	v_mfma_f32_16x16x32_f16 v[110:113], v[206:209], v[238:241], v[110:113]
	v_mfma_f32_16x16x32_f16 v[114:117], v[214:217], v[230:233], v[114:117]
	v_mfma_f32_16x16x32_f16 v[118:121], v[214:217], v[238:241], v[118:121]
	v_mfma_f32_16x16x32_f16 v[122:125], v[222:225], v[230:233], v[122:125]
	v_mfma_f32_16x16x32_f16 v[126:129], v[222:225], v[238:241], v[126:129]
	v_mfma_f32_16x16x32_f16 v[98:101], v[202:205], v[234:237], v[98:101]
	v_mfma_f32_16x16x32_f16 v[102:105], v[202:205], v[242:245], v[102:105]
	v_mfma_f32_16x16x32_f16 v[106:109], v[210:213], v[234:237], v[106:109]
	v_mfma_f32_16x16x32_f16 v[110:113], v[210:213], v[242:245], v[110:113]
	v_mfma_f32_16x16x32_f16 v[114:117], v[218:221], v[234:237], v[114:117]
	v_mfma_f32_16x16x32_f16 v[118:121], v[218:221], v[242:245], v[118:121]
	v_mfma_f32_16x16x32_f16 v[122:125], v[226:229], v[234:237], v[122:125]
	v_mfma_f32_16x16x32_f16 v[126:129], v[226:229], v[242:245], v[126:129]
	s_barrier
	ds_read_b128 v[176:179], v144
	ds_read_b128 v[180:183], v145
	ds_read_b128 v[184:187], v150
	ds_read_b128 v[188:191], v151
	v_readfirstlane_b32 s45, v156
	v_lshl_add_u64 v[230:231], v[192:193], 0, s[28:29]
	s_mov_b32 m0, s45
	v_readfirstlane_b32 s45, v157
	ds_read_b128 v[198:201], v173 offset:32768
	ds_read_b128 v[202:205], v173 offset:33792
	ds_read_b128 v[206:209], v173 offset:34816
	ds_read_b128 v[210:213], v173 offset:35840
	ds_read_b128 v[214:217], v173 offset:36864
	ds_read_b128 v[218:221], v173 offset:37888
	ds_read_b128 v[222:225], v173 offset:38912
	ds_read_b128 v[226:229], v173 offset:39936
	global_load_lds_dwordx4 v[230:231], off
	v_lshl_add_u64 v[230:231], v[246:247], 0, s[28:29]
	s_mov_b32 m0, s45
	s_nop 0
	global_load_lds_dwordx4 v[230:231], off
	s_waitcnt lgkmcnt(8)
	s_barrier
	s_waitcnt lgkmcnt(0)
	s_waitcnt lgkmcnt(0)
	v_mfma_f32_16x16x32_f16 v[2:5], v[198:201], v[176:179], v[2:5]
	v_mfma_f32_16x16x32_f16 v[6:9], v[198:201], v[184:187], v[6:9]
	v_mfma_f32_16x16x32_f16 v[10:13], v[206:209], v[176:179], v[10:13]
	v_mfma_f32_16x16x32_f16 v[18:21], v[206:209], v[184:187], v[18:21]
	v_mfma_f32_16x16x32_f16 v[30:33], v[214:217], v[176:179], v[30:33]
	v_mfma_f32_16x16x32_f16 v[42:45], v[214:217], v[184:187], v[42:45]
	v_mfma_f32_16x16x32_f16 v[54:57], v[222:225], v[176:179], v[54:57]
	v_mfma_f32_16x16x32_f16 v[66:69], v[222:225], v[184:187], v[66:69]
	v_mfma_f32_16x16x32_f16 v[2:5], v[202:205], v[180:183], v[2:5]
	v_mfma_f32_16x16x32_f16 v[6:9], v[202:205], v[188:191], v[6:9]
	v_mfma_f32_16x16x32_f16 v[10:13], v[210:213], v[180:183], v[10:13]
	v_mfma_f32_16x16x32_f16 v[18:21], v[210:213], v[188:191], v[18:21]
	v_mfma_f32_16x16x32_f16 v[30:33], v[218:221], v[180:183], v[30:33]
	v_mfma_f32_16x16x32_f16 v[42:45], v[218:221], v[188:191], v[42:45]
	v_mfma_f32_16x16x32_f16 v[54:57], v[226:229], v[180:183], v[54:57]
	v_mfma_f32_16x16x32_f16 v[66:69], v[226:229], v[188:191], v[66:69]
	s_barrier
	v_readfirstlane_b32 s45, v158
	v_lshl_add_u64 v[252:253], v[248:249], 0, s[30:31]
	s_mov_b32 m0, s45
	v_readfirstlane_b32 s45, v159
	ds_read_b128 v[230:233], v146
	ds_read_b128 v[234:237], v147
	ds_read_b128 v[238:241], v148
	ds_read_b128 v[242:245], v149
	global_load_lds_dwordx4 v[252:253], off
	v_lshl_add_u64 v[252:253], v[250:251], 0, s[30:31]
	s_mov_b32 m0, s45
	s_nop 0
	global_load_lds_dwordx4 v[252:253], off
	s_barrier
	s_waitcnt lgkmcnt(0)
	s_waitcnt lgkmcnt(0)
	v_mfma_f32_16x16x32_f16 v[14:17], v[198:201], v[230:233], v[14:17]
	v_mfma_f32_16x16x32_f16 v[22:25], v[198:201], v[238:241], v[22:25]
	v_mfma_f32_16x16x32_f16 v[34:37], v[206:209], v[230:233], v[34:37]
	v_mfma_f32_16x16x32_f16 v[46:49], v[206:209], v[238:241], v[46:49]
	v_mfma_f32_16x16x32_f16 v[58:61], v[214:217], v[230:233], v[58:61]
	v_mfma_f32_16x16x32_f16 v[70:73], v[214:217], v[238:241], v[70:73]
	v_mfma_f32_16x16x32_f16 v[78:81], v[222:225], v[230:233], v[78:81]
	v_mfma_f32_16x16x32_f16 v[86:89], v[222:225], v[238:241], v[86:89]
	v_mfma_f32_16x16x32_f16 v[14:17], v[202:205], v[234:237], v[14:17]
	v_mfma_f32_16x16x32_f16 v[22:25], v[202:205], v[242:245], v[22:25]
	v_mfma_f32_16x16x32_f16 v[34:37], v[210:213], v[234:237], v[34:37]
	v_mfma_f32_16x16x32_f16 v[46:49], v[210:213], v[242:245], v[46:49]
	v_mfma_f32_16x16x32_f16 v[58:61], v[218:221], v[234:237], v[58:61]
	v_mfma_f32_16x16x32_f16 v[70:73], v[218:221], v[242:245], v[70:73]
	v_mfma_f32_16x16x32_f16 v[78:81], v[226:229], v[234:237], v[78:81]
	v_mfma_f32_16x16x32_f16 v[86:89], v[226:229], v[242:245], v[86:89]
	v_readfirstlane_b32 s45, v160
	v_lshl_add_u64 v[192:193], v[192:193], 0, s[30:31]
	s_mov_b32 m0, s45
	v_readfirstlane_b32 s45, v165
	s_barrier
	ds_read_b128 v[198:201], v173 offset:49152
	ds_read_b128 v[202:205], v173 offset:50176
	ds_read_b128 v[206:209], v173 offset:51200
	ds_read_b128 v[210:213], v173 offset:52224
	ds_read_b128 v[214:217], v173 offset:53248
	ds_read_b128 v[218:221], v173 offset:54272
	ds_read_b128 v[222:225], v173 offset:55296
	ds_read_b128 v[226:229], v173 offset:56320
	global_load_lds_dwordx4 v[192:193], off
	v_lshl_add_u64 v[192:193], v[246:247], 0, s[30:31]
	s_mov_b32 m0, s45
	s_nop 0
	global_load_lds_dwordx4 v[192:193], off
	s_barrier
	s_waitcnt lgkmcnt(0)
	s_waitcnt lgkmcnt(0)
	v_mfma_f32_16x16x32_f16 v[26:29], v[198:201], v[176:179], v[26:29]
	v_mfma_f32_16x16x32_f16 v[38:41], v[198:201], v[184:187], v[38:41]
	v_mfma_f32_16x16x32_f16 v[50:53], v[206:209], v[176:179], v[50:53]
	v_mfma_f32_16x16x32_f16 v[62:65], v[206:209], v[184:187], v[62:65]
	v_mfma_f32_16x16x32_f16 v[74:77], v[214:217], v[176:179], v[74:77]
	v_mfma_f32_16x16x32_f16 v[82:85], v[214:217], v[184:187], v[82:85]
	v_mfma_f32_16x16x32_f16 v[90:93], v[222:225], v[176:179], v[90:93]
	v_mfma_f32_16x16x32_f16 v[94:97], v[222:225], v[184:187], v[94:97]
	v_mfma_f32_16x16x32_f16 v[26:29], v[202:205], v[180:183], v[26:29]
	v_mfma_f32_16x16x32_f16 v[38:41], v[202:205], v[188:191], v[38:41]
	v_mfma_f32_16x16x32_f16 v[50:53], v[210:213], v[180:183], v[50:53]
	v_mfma_f32_16x16x32_f16 v[62:65], v[210:213], v[188:191], v[62:65]
	v_mfma_f32_16x16x32_f16 v[74:77], v[218:221], v[180:183], v[74:77]
	v_mfma_f32_16x16x32_f16 v[82:85], v[218:221], v[188:191], v[82:85]
	v_mfma_f32_16x16x32_f16 v[90:93], v[226:229], v[180:183], v[90:93]
	v_mfma_f32_16x16x32_f16 v[94:97], v[226:229], v[188:191], v[94:97]
	s_barrier
	v_readfirstlane_b32 s45, v166
	v_lshl_add_u64 v[176:177], v[248:249], 0, s[34:35]
	s_mov_b32 m0, s45
	v_readfirstlane_b32 s45, v167
	global_load_lds_dwordx4 v[176:177], off
	v_lshl_add_u64 v[176:177], v[250:251], 0, s[34:35]
	s_mov_b32 m0, s45
	s_nop 0
	global_load_lds_dwordx4 v[176:177], off
	s_waitcnt vmcnt(6)
	s_barrier
	v_mfma_f32_16x16x32_f16 v[98:101], v[198:201], v[230:233], v[98:101]
	v_mfma_f32_16x16x32_f16 v[102:105], v[198:201], v[238:241], v[102:105]
	v_mfma_f32_16x16x32_f16 v[106:109], v[206:209], v[230:233], v[106:109]
	v_mfma_f32_16x16x32_f16 v[110:113], v[206:209], v[238:241], v[110:113]
	v_mfma_f32_16x16x32_f16 v[114:117], v[214:217], v[230:233], v[114:117]
	v_mfma_f32_16x16x32_f16 v[118:121], v[214:217], v[238:241], v[118:121]
	v_mfma_f32_16x16x32_f16 v[122:125], v[222:225], v[230:233], v[122:125]
	v_mfma_f32_16x16x32_f16 v[126:129], v[222:225], v[238:241], v[126:129]
	v_mfma_f32_16x16x32_f16 v[98:101], v[202:205], v[234:237], v[98:101]
	v_mfma_f32_16x16x32_f16 v[102:105], v[202:205], v[242:245], v[102:105]
	v_mfma_f32_16x16x32_f16 v[106:109], v[210:213], v[234:237], v[106:109]
	v_mfma_f32_16x16x32_f16 v[110:113], v[210:213], v[242:245], v[110:113]
	v_mfma_f32_16x16x32_f16 v[114:117], v[218:221], v[234:237], v[114:117]
	v_mfma_f32_16x16x32_f16 v[118:121], v[218:221], v[242:245], v[118:121]
	v_mfma_f32_16x16x32_f16 v[122:125], v[226:229], v[234:237], v[122:125]
	v_mfma_f32_16x16x32_f16 v[126:129], v[226:229], v[242:245], v[126:129]
	s_add_i32 s44, s44, 2
	s_add_u32 s42, s42, 0x100
	s_addc_u32 s43, s43, 0
	s_cmp_lt_u32 s44, 4
	s_barrier
	s_cbranch_scc1 .LBB9_38
	s_add_u32 s40, s40, 0x20380
	s_addc_u32 s41, s41, 0
	v_readfirstlane_b32 s39, v174
	v_lshl_add_u64 v[130:131], v[130:131], 1, s[40:41]
	s_mov_b32 m0, s39
	v_readfirstlane_b32 s39, v175
	ds_read_b128 v[134:137], v169
	ds_read_b128 v[138:141], v170
	ds_read_b128 v[152:155], v171
	ds_read_b128 v[156:159], v172
	ds_read_b128 v[166:169], v173
	ds_read_b128 v[176:179], v173 offset:1024
	ds_read_b128 v[180:183], v173 offset:2048
	ds_read_b128 v[184:187], v173 offset:3072
	ds_read_b128 v[188:191], v173 offset:4096
	ds_read_b128 v[198:201], v173 offset:5120
	ds_read_b128 v[202:205], v173 offset:6144
	ds_read_b128 v[206:209], v173 offset:7168
	global_load_lds_dwordx4 v[130:131], off
	v_lshl_add_u64 v[130:131], v[132:133], 1, s[40:41]
	s_mov_b32 m0, s39
	s_nop 0
	global_load_lds_dwordx4 v[130:131], off
	s_barrier
	s_waitcnt lgkmcnt(0)
	s_waitcnt lgkmcnt(0)
	v_mfma_f32_16x16x32_f16 v[2:5], v[166:169], v[134:137], v[2:5]
	v_mfma_f32_16x16x32_f16 v[6:9], v[166:169], v[152:155], v[6:9]
	v_mfma_f32_16x16x32_f16 v[30:33], v[188:191], v[134:137], v[30:33]
	v_mfma_f32_16x16x32_f16 v[2:5], v[176:179], v[138:141], v[2:5]
	v_mfma_f32_16x16x32_f16 v[6:9], v[176:179], v[156:159], v[6:9]
	v_mfma_f32_16x16x32_f16 v[10:13], v[180:183], v[134:137], v[10:13]
	v_mfma_f32_16x16x32_f16 v[18:21], v[180:183], v[152:155], v[18:21]
	v_mfma_f32_16x16x32_f16 v[30:33], v[198:201], v[138:141], v[30:33]
	v_mfma_f32_16x16x32_f16 v[42:45], v[188:191], v[152:155], v[42:45]
	v_mfma_f32_16x16x32_f16 v[54:57], v[202:205], v[134:137], v[54:57]
	v_mfma_f32_16x16x32_f16 v[66:69], v[202:205], v[152:155], v[66:69]
	v_mfma_f32_16x16x32_f16 v[10:13], v[184:187], v[138:141], v[10:13]
	v_mfma_f32_16x16x32_f16 v[18:21], v[184:187], v[156:159], v[18:21]
	v_mfma_f32_16x16x32_f16 v[42:45], v[198:201], v[156:159], v[42:45]
	v_mfma_f32_16x16x32_f16 v[54:57], v[206:209], v[138:141], v[54:57]
	v_mfma_f32_16x16x32_f16 v[66:69], v[206:209], v[156:159], v[66:69]
	s_barrier
	ds_read_b128 v[130:133], v161
	ds_read_b128 v[210:213], v162
	ds_read_b128 v[160:163], v163
	ds_read_b128 v[214:217], v164
	s_barrier
	s_waitcnt lgkmcnt(0)
	s_waitcnt lgkmcnt(0)
	v_mfma_f32_16x16x32_f16 v[58:61], v[188:191], v[130:133], v[58:61]
	v_mfma_f32_16x16x32_f16 v[14:17], v[166:169], v[130:133], v[14:17]
	v_mfma_f32_16x16x32_f16 v[22:25], v[166:169], v[160:163], v[22:25]
	v_mfma_f32_16x16x32_f16 v[164:167], v[198:201], v[210:213], v[58:61]
	v_mfma_f32_16x16x32_f16 v[58:61], v[188:191], v[160:163], v[70:73]
	v_mfma_f32_16x16x32_f16 v[46:49], v[180:183], v[160:163], v[46:49]
	v_mfma_f32_16x16x32_f16 v[168:171], v[198:201], v[214:217], v[58:61]
	v_mfma_f32_16x16x32_f16 v[58:61], v[202:205], v[130:133], v[78:81]
	v_mfma_f32_16x16x32_f16 v[14:17], v[176:179], v[210:213], v[14:17]
	v_mfma_f32_16x16x32_f16 v[34:37], v[180:183], v[130:133], v[34:37]
	v_mfma_f32_16x16x32_f16 v[46:49], v[184:187], v[214:217], v[46:49]
	v_mfma_f32_16x16x32_f16 v[78:81], v[206:209], v[210:213], v[58:61]
	v_mfma_f32_16x16x32_f16 v[58:61], v[202:205], v[160:163], v[86:89]
	v_mfma_f32_16x16x32_f16 v[22:25], v[176:179], v[214:217], v[22:25]
	v_mfma_f32_16x16x32_f16 v[34:37], v[184:187], v[210:213], v[34:37]
	v_mfma_f32_16x16x32_f16 v[86:89], v[206:209], v[214:217], v[58:61]
	s_barrier
	s_nop 2
	ds_read_b128 v[58:61], v173 offset:16384
	ds_read_b128 v[70:73], v173 offset:17408
	ds_read_b128 v[174:177], v173 offset:18432
	ds_read_b128 v[178:181], v173 offset:19456
	ds_read_b128 v[182:185], v173 offset:20480
	ds_read_b128 v[186:189], v173 offset:21504
	ds_read_b128 v[190:193], v173 offset:22528
	ds_read_b128 v[198:201], v173 offset:23552
	s_waitcnt vmcnt(4)
	s_barrier
	s_waitcnt lgkmcnt(0)
	s_waitcnt lgkmcnt(0)
	v_mfma_f32_16x16x32_f16 v[26:29], v[58:61], v[134:137], v[26:29]
	v_mfma_f32_16x16x32_f16 v[26:29], v[70:73], v[138:141], v[26:29]
	v_mfma_f32_16x16x32_f16 v[38:41], v[58:61], v[152:155], v[38:41]
	v_mfma_f32_16x16x32_f16 v[50:53], v[174:177], v[134:137], v[50:53]
	v_mfma_f32_16x16x32_f16 v[62:65], v[174:177], v[152:155], v[62:65]
	v_mfma_f32_16x16x32_f16 v[74:77], v[182:185], v[134:137], v[74:77]
	v_mfma_f32_16x16x32_f16 v[82:85], v[182:185], v[152:155], v[82:85]
	v_mfma_f32_16x16x32_f16 v[90:93], v[190:193], v[134:137], v[90:93]
	v_mfma_f32_16x16x32_f16 v[94:97], v[190:193], v[152:155], v[94:97]
	v_mfma_f32_16x16x32_f16 v[38:41], v[70:73], v[156:159], v[38:41]
	v_mfma_f32_16x16x32_f16 v[50:53], v[178:181], v[138:141], v[50:53]
	v_mfma_f32_16x16x32_f16 v[62:65], v[178:181], v[156:159], v[62:65]
	v_mfma_f32_16x16x32_f16 v[74:77], v[186:189], v[138:141], v[74:77]
	v_mfma_f32_16x16x32_f16 v[82:85], v[186:189], v[156:159], v[82:85]
	v_mfma_f32_16x16x32_f16 v[90:93], v[198:201], v[138:141], v[90:93]
	v_mfma_f32_16x16x32_f16 v[94:97], v[198:201], v[156:159], v[94:97]
	v_mfma_f32_16x16x32_f16 v[98:101], v[58:61], v[130:133], v[98:101]
	v_mfma_f32_16x16x32_f16 v[58:61], v[58:61], v[160:163], v[102:105]
	v_mfma_f32_16x16x32_f16 v[102:105], v[70:73], v[214:217], v[58:61]
	v_mfma_f32_16x16x32_f16 v[58:61], v[174:177], v[130:133], v[106:109]
	v_mfma_f32_16x16x32_f16 v[106:109], v[178:181], v[210:213], v[58:61]
	v_mfma_f32_16x16x32_f16 v[58:61], v[174:177], v[160:163], v[110:113]
	v_mfma_f32_16x16x32_f16 v[202:205], v[178:181], v[214:217], v[58:61]
	v_mfma_f32_16x16x32_f16 v[58:61], v[182:185], v[130:133], v[114:117]
	v_mfma_f32_16x16x32_f16 v[206:209], v[186:189], v[210:213], v[58:61]
	v_mfma_f32_16x16x32_f16 v[58:61], v[182:185], v[160:163], v[118:121]
	v_mfma_f32_16x16x32_f16 v[218:221], v[186:189], v[214:217], v[58:61]
	v_mfma_f32_16x16x32_f16 v[58:61], v[190:193], v[130:133], v[122:125]
	v_mfma_f32_16x16x32_f16 v[98:101], v[70:73], v[210:213], v[98:101]
	v_mfma_f32_16x16x32_f16 v[210:213], v[198:201], v[210:213], v[58:61]
	v_mfma_f32_16x16x32_f16 v[58:61], v[190:193], v[160:163], v[126:129]
	v_mfma_f32_16x16x32_f16 v[198:201], v[198:201], v[214:217], v[58:61]
	s_barrier
	ds_read_b128 v[110:113], v144
	ds_read_b128 v[130:133], v145
	ds_read_b128 v[214:217], v150
	ds_read_b128 v[222:225], v151
	s_nop 0
	ds_read_b128 v[58:61], v173 offset:32768
	ds_read_b128 v[70:73], v173 offset:33792
	ds_read_b128 v[114:117], v173 offset:34816
	ds_read_b128 v[118:121], v173 offset:35840
	ds_read_b128 v[134:137], v173 offset:36864
	ds_read_b128 v[138:141], v173 offset:37888
	ds_read_b128 v[178:181], v173 offset:38912
	ds_read_b128 v[226:229], v173 offset:39936
	s_waitcnt vmcnt(2)
	s_barrier
	s_waitcnt lgkmcnt(0)
	s_waitcnt lgkmcnt(0)
	v_mfma_f32_16x16x32_f16 v[2:5], v[58:61], v[110:113], v[2:5]
	v_mfma_f32_16x16x32_f16 v[190:193], v[70:73], v[130:133], v[2:5]
	v_mfma_f32_16x16x32_f16 v[2:5], v[58:61], v[214:217], v[6:9]
	v_mfma_f32_16x16x32_f16 v[158:161], v[70:73], v[222:225], v[2:5]
	v_mfma_f32_16x16x32_f16 v[2:5], v[114:117], v[110:113], v[10:13]
	v_mfma_f32_16x16x32_f16 v[186:189], v[118:121], v[130:133], v[2:5]
	v_mfma_f32_16x16x32_f16 v[2:5], v[114:117], v[214:217], v[18:21]
	v_mfma_f32_16x16x32_f16 v[154:157], v[118:121], v[222:225], v[2:5]
	v_mfma_f32_16x16x32_f16 v[2:5], v[134:137], v[110:113], v[30:33]
	v_mfma_f32_16x16x32_f16 v[182:185], v[138:141], v[130:133], v[2:5]
	v_mfma_f32_16x16x32_f16 v[2:5], v[134:137], v[214:217], v[42:45]
	v_mfma_f32_16x16x32_f16 v[150:153], v[138:141], v[222:225], v[2:5]
	v_mfma_f32_16x16x32_f16 v[2:5], v[178:181], v[110:113], v[54:57]
	v_mfma_f32_16x16x32_f16 v[174:177], v[226:229], v[130:133], v[2:5]
	v_mfma_f32_16x16x32_f16 v[2:5], v[178:181], v[214:217], v[66:69]
	v_mfma_f32_16x16x32_f16 v[142:145], v[226:229], v[222:225], v[2:5]
	s_barrier
	s_nop 4
	ds_read_b128 v[2:5], v146
	ds_read_b128 v[10:13], v147
	ds_read_b128 v[18:21], v148
	ds_read_b128 v[42:45], v149
	s_waitcnt vmcnt(0)
	s_barrier
	s_waitcnt lgkmcnt(0)
	s_waitcnt lgkmcnt(0)
	v_mfma_f32_16x16x32_f16 v[6:9], v[58:61], v[2:5], v[14:17]
	v_mfma_f32_16x16x32_f16 v[126:129], v[70:73], v[10:13], v[6:9]
	v_mfma_f32_16x16x32_f16 v[6:9], v[58:61], v[18:21], v[22:25]
	v_mfma_f32_16x16x32_f16 v[70:73], v[70:73], v[42:45], v[6:9]
	v_mfma_f32_16x16x32_f16 v[6:9], v[114:117], v[2:5], v[34:37]
	v_mfma_f32_16x16x32_f16 v[122:125], v[118:121], v[10:13], v[6:9]
	v_mfma_f32_16x16x32_f16 v[6:9], v[114:117], v[18:21], v[46:49]
	v_mfma_f32_16x16x32_f16 v[58:61], v[118:121], v[42:45], v[6:9]
	v_mfma_f32_16x16x32_f16 v[6:9], v[134:137], v[2:5], v[164:167]
	v_mfma_f32_16x16x32_f16 v[118:121], v[138:141], v[10:13], v[6:9]
	v_mfma_f32_16x16x32_f16 v[6:9], v[134:137], v[18:21], v[168:171]
	v_mfma_f32_16x16x32_f16 v[46:49], v[138:141], v[42:45], v[6:9]
	v_mfma_f32_16x16x32_f16 v[6:9], v[178:181], v[2:5], v[78:81]
	v_mfma_f32_16x16x32_f16 v[114:117], v[226:229], v[10:13], v[6:9]
	v_mfma_f32_16x16x32_f16 v[6:9], v[178:181], v[18:21], v[86:89]
	v_mfma_f32_16x16x32_f16 v[30:33], v[226:229], v[42:45], v[6:9]
	s_barrier
	s_nop 4
	ds_read_b128 v[6:9], v173 offset:49152
	ds_read_b128 v[14:17], v173 offset:50176
	ds_read_b128 v[22:25], v173 offset:51200
	ds_read_b128 v[34:37], v173 offset:52224
	ds_read_b128 v[54:57], v173 offset:53248
	ds_read_b128 v[66:69], v173 offset:54272
	ds_read_b128 v[78:81], v173 offset:55296
	ds_read_b128 v[86:89], v173 offset:56320
	s_barrier
	s_waitcnt lgkmcnt(0)
	s_waitcnt lgkmcnt(0)
	v_mfma_f32_16x16x32_f16 v[26:29], v[6:9], v[110:113], v[26:29]
	v_mfma_f32_16x16x32_f16 v[178:181], v[14:17], v[130:133], v[26:29]
	v_mfma_f32_16x16x32_f16 v[26:29], v[6:9], v[214:217], v[38:41]
	v_mfma_f32_16x16x32_f16 v[146:149], v[14:17], v[222:225], v[26:29]
	v_mfma_f32_16x16x32_f16 v[26:29], v[22:25], v[110:113], v[50:53]
	v_mfma_f32_16x16x32_f16 v[170:173], v[34:37], v[130:133], v[26:29]
	v_mfma_f32_16x16x32_f16 v[26:29], v[22:25], v[214:217], v[62:65]
	v_mfma_f32_16x16x32_f16 v[138:141], v[34:37], v[222:225], v[26:29]
	v_mfma_f32_16x16x32_f16 v[26:29], v[54:57], v[110:113], v[74:77]
	v_mfma_f32_16x16x32_f16 v[166:169], v[66:69], v[130:133], v[26:29]
	v_mfma_f32_16x16x32_f16 v[26:29], v[54:57], v[214:217], v[82:85]
	v_mfma_f32_16x16x32_f16 v[134:137], v[66:69], v[222:225], v[26:29]
	v_mfma_f32_16x16x32_f16 v[26:29], v[78:81], v[110:113], v[90:93]
	v_mfma_f32_16x16x32_f16 v[162:165], v[86:89], v[130:133], v[26:29]
	v_mfma_f32_16x16x32_f16 v[26:29], v[78:81], v[214:217], v[94:97]
	v_mfma_f32_16x16x32_f16 v[130:133], v[86:89], v[222:225], v[26:29]
	v_mfma_f32_16x16x32_f16 v[26:29], v[6:9], v[2:5], v[98:101]
	v_mfma_f32_16x16x32_f16 v[6:9], v[6:9], v[18:21], v[102:105]
	v_mfma_f32_16x16x32_f16 v[110:113], v[14:17], v[10:13], v[26:29]
	v_mfma_f32_16x16x32_f16 v[26:29], v[14:17], v[42:45], v[6:9]
	v_mfma_f32_16x16x32_f16 v[6:9], v[22:25], v[2:5], v[106:109]
	v_mfma_f32_16x16x32_f16 v[106:109], v[34:37], v[10:13], v[6:9]
	v_mfma_f32_16x16x32_f16 v[6:9], v[22:25], v[18:21], v[202:205]
	v_mfma_f32_16x16x32_f16 v[14:17], v[34:37], v[42:45], v[6:9]
	v_mfma_f32_16x16x32_f16 v[6:9], v[54:57], v[2:5], v[206:209]
	v_mfma_f32_16x16x32_f16 v[2:5], v[78:81], v[2:5], v[210:213]
	v_mfma_f32_16x16x32_f16 v[102:105], v[66:69], v[10:13], v[6:9]
	v_mfma_f32_16x16x32_f16 v[6:9], v[54:57], v[18:21], v[218:221]
	v_mfma_f32_16x16x32_f16 v[98:101], v[86:89], v[10:13], v[2:5]
	v_mfma_f32_16x16x32_f16 v[2:5], v[78:81], v[18:21], v[198:201]
	v_mfma_f32_16x16x32_f16 v[6:9], v[66:69], v[42:45], v[6:9]
	v_mfma_f32_16x16x32_f16 v[2:5], v[86:89], v[42:45], v[2:5]
	s_cmpk_gt_u32 s54, 0xff
	s_barrier
	s_cbranch_scc1 .LBB9_34
	s_barrier
	s_branch .LBB9_34

.LBB10_12:
	ds_read_b128 v[182:185], v171
	ds_read_b128 v[186:189], v173
	ds_read_b128 v[190:193], v174
	ds_read_b128 v[194:197], v175
	v_add_u32_e32 v177, 0xc000, v148
	v_lshl_add_u64 v[246:247], v[136:137], 0, s[44:45]
	v_readfirstlane_b32 s47, v177
	v_add_u32_e32 v176, s63, v170
	v_lshl_add_u64 v[178:179], v[246:247], 0, s[28:29]
	s_mov_b32 m0, s47
	ds_read_b128 v[198:201], v176
	ds_read_b128 v[202:205], v176 offset:1024
	ds_read_b128 v[206:209], v176 offset:2048
	ds_read_b128 v[210:213], v176 offset:3072
	ds_read_b128 v[214:217], v176 offset:4096
	ds_read_b128 v[218:221], v176 offset:5120
	ds_read_b128 v[222:225], v176 offset:6144
	ds_read_b128 v[226:229], v176 offset:7168
	global_load_lds_dwordx4 v[178:179], off
	v_add_u32_e32 v178, 0xe000, v148
	v_lshl_add_u64 v[248:249], v[134:135], 0, s[44:45]
	v_readfirstlane_b32 s47, v178
	v_lshl_add_u64 v[230:231], v[248:249], 0, s[28:29]
	s_mov_b32 m0, s47
	s_nop 0
	global_load_lds_dwordx4 v[230:231], off
	s_waitcnt lgkmcnt(8)
	s_barrier
	s_waitcnt lgkmcnt(0)
	s_waitcnt lgkmcnt(0)
	v_mfma_f32_16x16x32_f16 v[126:129], v[198:201], v[182:185], v[126:129]
	v_mfma_f32_16x16x32_f16 v[122:125], v[198:201], v[190:193], v[122:125]
	v_mfma_f32_16x16x32_f16 v[118:121], v[206:209], v[182:185], v[118:121]
	v_mfma_f32_16x16x32_f16 v[114:117], v[206:209], v[190:193], v[114:117]
	v_mfma_f32_16x16x32_f16 v[110:113], v[214:217], v[182:185], v[110:113]
	v_mfma_f32_16x16x32_f16 v[106:109], v[214:217], v[190:193], v[106:109]
	v_mfma_f32_16x16x32_f16 v[102:105], v[222:225], v[182:185], v[102:105]
	v_mfma_f32_16x16x32_f16 v[98:101], v[222:225], v[190:193], v[98:101]
	v_mfma_f32_16x16x32_f16 v[126:129], v[202:205], v[186:189], v[126:129]
	v_mfma_f32_16x16x32_f16 v[122:125], v[202:205], v[194:197], v[122:125]
	v_mfma_f32_16x16x32_f16 v[118:121], v[210:213], v[186:189], v[118:121]
	v_mfma_f32_16x16x32_f16 v[114:117], v[210:213], v[194:197], v[114:117]
	v_mfma_f32_16x16x32_f16 v[110:113], v[218:221], v[186:189], v[110:113]
	v_mfma_f32_16x16x32_f16 v[106:109], v[218:221], v[194:197], v[106:109]
	v_mfma_f32_16x16x32_f16 v[102:105], v[226:229], v[186:189], v[102:105]
	v_mfma_f32_16x16x32_f16 v[98:101], v[226:229], v[194:197], v[98:101]
	s_barrier
	v_lshl_add_u64 v[250:251], v[140:141], 0, s[44:45]
	v_readfirstlane_b32 s47, v142
	v_lshl_add_u64 v[252:253], v[250:251], 0, s[30:31]
	s_mov_b32 m0, s47
	ds_read_b128 v[230:233], v162
	ds_read_b128 v[234:237], v163
	ds_read_b128 v[238:241], v164
	ds_read_b128 v[242:245], v165
	global_load_lds_dwordx4 v[252:253], off
	v_lshl_add_u64 v[252:253], v[138:139], 0, s[44:45]
	v_readfirstlane_b32 s47, v143
	v_lshl_add_u64 v[254:255], v[252:253], 0, s[30:31]
	s_mov_b32 m0, s47
	s_nop 0
	global_load_lds_dwordx4 v[254:255], off
	s_barrier
	s_waitcnt lgkmcnt(0)
	s_waitcnt lgkmcnt(0)
	v_mfma_f32_16x16x32_f16 v[94:97], v[198:201], v[230:233], v[94:97]
	v_mfma_f32_16x16x32_f16 v[90:93], v[198:201], v[238:241], v[90:93]
	v_mfma_f32_16x16x32_f16 v[86:89], v[206:209], v[230:233], v[86:89]
	v_mfma_f32_16x16x32_f16 v[82:85], v[206:209], v[238:241], v[82:85]
	v_mfma_f32_16x16x32_f16 v[78:81], v[214:217], v[230:233], v[78:81]
	v_mfma_f32_16x16x32_f16 v[74:77], v[214:217], v[238:241], v[74:77]
	v_mfma_f32_16x16x32_f16 v[70:73], v[222:225], v[230:233], v[70:73]
	v_mfma_f32_16x16x32_f16 v[66:69], v[222:225], v[238:241], v[66:69]
	v_mfma_f32_16x16x32_f16 v[94:97], v[202:205], v[234:237], v[94:97]
	v_mfma_f32_16x16x32_f16 v[90:93], v[202:205], v[242:245], v[90:93]
	v_mfma_f32_16x16x32_f16 v[86:89], v[210:213], v[234:237], v[86:89]
	v_mfma_f32_16x16x32_f16 v[82:85], v[210:213], v[242:245], v[82:85]
	v_mfma_f32_16x16x32_f16 v[78:81], v[218:221], v[234:237], v[78:81]
	v_mfma_f32_16x16x32_f16 v[74:77], v[218:221], v[242:245], v[74:77]
	v_mfma_f32_16x16x32_f16 v[70:73], v[226:229], v[234:237], v[70:73]
	v_mfma_f32_16x16x32_f16 v[66:69], v[226:229], v[242:245], v[66:69]
	v_readfirstlane_b32 s47, v148
	v_lshl_add_u64 v[254:255], v[246:247], 0, s[30:31]
	s_mov_b32 m0, s47
	v_readfirstlane_b32 s47, v149
	s_barrier
	ds_read_b128 v[198:201], v176 offset:16384
	ds_read_b128 v[202:205], v176 offset:17408
	ds_read_b128 v[206:209], v176 offset:18432
	ds_read_b128 v[210:213], v176 offset:19456
	ds_read_b128 v[214:217], v176 offset:20480
	ds_read_b128 v[218:221], v176 offset:21504
	ds_read_b128 v[222:225], v176 offset:22528
	ds_read_b128 v[226:229], v176 offset:23552
	global_load_lds_dwordx4 v[254:255], off
	v_lshl_add_u64 v[254:255], v[248:249], 0, s[30:31]
	s_mov_b32 m0, s47
	s_nop 0
	global_load_lds_dwordx4 v[254:255], off
	s_barrier
	s_waitcnt lgkmcnt(0)
	s_waitcnt lgkmcnt(0)
	v_mfma_f32_16x16x32_f16 v[62:65], v[198:201], v[182:185], v[62:65]
	v_mfma_f32_16x16x32_f16 v[58:61], v[198:201], v[190:193], v[58:61]
	v_mfma_f32_16x16x32_f16 v[54:57], v[206:209], v[182:185], v[54:57]
	v_mfma_f32_16x16x32_f16 v[50:53], v[206:209], v[190:193], v[50:53]
	v_mfma_f32_16x16x32_f16 v[46:49], v[214:217], v[182:185], v[46:49]
	v_mfma_f32_16x16x32_f16 v[42:45], v[214:217], v[190:193], v[42:45]
	v_mfma_f32_16x16x32_f16 v[38:41], v[222:225], v[182:185], v[38:41]
	v_mfma_f32_16x16x32_f16 v[34:37], v[222:225], v[190:193], v[34:37]
	v_mfma_f32_16x16x32_f16 v[62:65], v[202:205], v[186:189], v[62:65]
	v_mfma_f32_16x16x32_f16 v[58:61], v[202:205], v[194:197], v[58:61]
	v_mfma_f32_16x16x32_f16 v[54:57], v[210:213], v[186:189], v[54:57]
	v_mfma_f32_16x16x32_f16 v[50:53], v[210:213], v[194:197], v[50:53]
	v_mfma_f32_16x16x32_f16 v[46:49], v[218:221], v[186:189], v[46:49]
	v_mfma_f32_16x16x32_f16 v[42:45], v[218:221], v[194:197], v[42:45]
	v_mfma_f32_16x16x32_f16 v[38:41], v[226:229], v[186:189], v[38:41]
	v_mfma_f32_16x16x32_f16 v[34:37], v[226:229], v[194:197], v[34:37]
	s_barrier
	v_readfirstlane_b32 s47, v154
	v_lshl_add_u64 v[182:183], v[250:251], 0, s[34:35]
	s_mov_b32 m0, s47
	v_readfirstlane_b32 s47, v155
	global_load_lds_dwordx4 v[182:183], off
	v_lshl_add_u64 v[182:183], v[252:253], 0, s[34:35]
	s_mov_b32 m0, s47
	s_nop 0
	global_load_lds_dwordx4 v[182:183], off
	s_waitcnt vmcnt(6)
	s_barrier
	v_mfma_f32_16x16x32_f16 v[30:33], v[198:201], v[230:233], v[30:33]
	v_mfma_f32_16x16x32_f16 v[26:29], v[198:201], v[238:241], v[26:29]
	v_mfma_f32_16x16x32_f16 v[22:25], v[206:209], v[230:233], v[22:25]
	v_mfma_f32_16x16x32_f16 v[18:21], v[206:209], v[238:241], v[18:21]
	v_mfma_f32_16x16x32_f16 v[14:17], v[214:217], v[230:233], v[14:17]
	v_mfma_f32_16x16x32_f16 v[10:13], v[214:217], v[238:241], v[10:13]
	v_mfma_f32_16x16x32_f16 v[6:9], v[222:225], v[230:233], v[6:9]
	v_mfma_f32_16x16x32_f16 v[2:5], v[222:225], v[238:241], v[2:5]
	v_mfma_f32_16x16x32_f16 v[30:33], v[202:205], v[234:237], v[30:33]
	v_mfma_f32_16x16x32_f16 v[26:29], v[202:205], v[242:245], v[26:29]
	v_mfma_f32_16x16x32_f16 v[22:25], v[210:213], v[234:237], v[22:25]
	v_mfma_f32_16x16x32_f16 v[18:21], v[210:213], v[242:245], v[18:21]
	v_mfma_f32_16x16x32_f16 v[14:17], v[218:221], v[234:237], v[14:17]
	v_mfma_f32_16x16x32_f16 v[10:13], v[218:221], v[242:245], v[10:13]
	v_mfma_f32_16x16x32_f16 v[6:9], v[226:229], v[234:237], v[6:9]
	v_mfma_f32_16x16x32_f16 v[2:5], v[226:229], v[242:245], v[2:5]
	s_barrier
	ds_read_b128 v[182:185], v144
	ds_read_b128 v[186:189], v145
	ds_read_b128 v[190:193], v146
	ds_read_b128 v[194:197], v147
	v_readfirstlane_b32 s47, v156
	v_lshl_add_u64 v[230:231], v[246:247], 0, s[34:35]
	s_mov_b32 m0, s47
	v_readfirstlane_b32 s47, v157
	ds_read_b128 v[198:201], v176 offset:32768
	ds_read_b128 v[202:205], v176 offset:33792
	ds_read_b128 v[206:209], v176 offset:34816
	ds_read_b128 v[210:213], v176 offset:35840
	ds_read_b128 v[214:217], v176 offset:36864
	ds_read_b128 v[218:221], v176 offset:37888
	ds_read_b128 v[222:225], v176 offset:38912
	ds_read_b128 v[226:229], v176 offset:39936
	global_load_lds_dwordx4 v[230:231], off
	v_lshl_add_u64 v[230:231], v[248:249], 0, s[34:35]
	s_mov_b32 m0, s47
	s_nop 0
	global_load_lds_dwordx4 v[230:231], off
	s_waitcnt lgkmcnt(8)
	s_barrier
	s_waitcnt lgkmcnt(0)
	s_waitcnt lgkmcnt(0)
	v_mfma_f32_16x16x32_f16 v[126:129], v[198:201], v[182:185], v[126:129]
	v_mfma_f32_16x16x32_f16 v[122:125], v[198:201], v[190:193], v[122:125]
	v_mfma_f32_16x16x32_f16 v[118:121], v[206:209], v[182:185], v[118:121]
	v_mfma_f32_16x16x32_f16 v[114:117], v[206:209], v[190:193], v[114:117]
	v_mfma_f32_16x16x32_f16 v[110:113], v[214:217], v[182:185], v[110:113]
	v_mfma_f32_16x16x32_f16 v[106:109], v[214:217], v[190:193], v[106:109]
	v_mfma_f32_16x16x32_f16 v[102:105], v[222:225], v[182:185], v[102:105]
	v_mfma_f32_16x16x32_f16 v[98:101], v[222:225], v[190:193], v[98:101]
	v_mfma_f32_16x16x32_f16 v[126:129], v[202:205], v[186:189], v[126:129]
	v_mfma_f32_16x16x32_f16 v[122:125], v[202:205], v[194:197], v[122:125]
	v_mfma_f32_16x16x32_f16 v[118:121], v[210:213], v[186:189], v[118:121]
	v_mfma_f32_16x16x32_f16 v[114:117], v[210:213], v[194:197], v[114:117]
	v_mfma_f32_16x16x32_f16 v[110:113], v[218:221], v[186:189], v[110:113]
	v_mfma_f32_16x16x32_f16 v[106:109], v[218:221], v[194:197], v[106:109]
	v_mfma_f32_16x16x32_f16 v[102:105], v[226:229], v[186:189], v[102:105]
	v_mfma_f32_16x16x32_f16 v[98:101], v[226:229], v[194:197], v[98:101]
	s_barrier
	v_readfirstlane_b32 s47, v158
	v_lshl_add_u64 v[254:255], v[250:251], 0, s[36:37]
	s_mov_b32 m0, s47
	v_readfirstlane_b32 s47, v160
	ds_read_b128 v[230:233], v150
	ds_read_b128 v[234:237], v151
	ds_read_b128 v[238:241], v152
	ds_read_b128 v[242:245], v153
	global_load_lds_dwordx4 v[254:255], off
	v_lshl_add_u64 v[254:255], v[252:253], 0, s[36:37]
	s_mov_b32 m0, s47
	s_nop 0
	global_load_lds_dwordx4 v[254:255], off
	s_barrier
	s_waitcnt lgkmcnt(0)
	s_waitcnt lgkmcnt(0)
	v_mfma_f32_16x16x32_f16 v[94:97], v[198:201], v[230:233], v[94:97]
	v_mfma_f32_16x16x32_f16 v[90:93], v[198:201], v[238:241], v[90:93]
	v_mfma_f32_16x16x32_f16 v[86:89], v[206:209], v[230:233], v[86:89]
	v_mfma_f32_16x16x32_f16 v[82:85], v[206:209], v[238:241], v[82:85]
	v_mfma_f32_16x16x32_f16 v[78:81], v[214:217], v[230:233], v[78:81]
	v_mfma_f32_16x16x32_f16 v[74:77], v[214:217], v[238:241], v[74:77]
	v_mfma_f32_16x16x32_f16 v[70:73], v[222:225], v[230:233], v[70:73]
	v_mfma_f32_16x16x32_f16 v[66:69], v[222:225], v[238:241], v[66:69]
	v_mfma_f32_16x16x32_f16 v[94:97], v[202:205], v[234:237], v[94:97]
	v_mfma_f32_16x16x32_f16 v[90:93], v[202:205], v[242:245], v[90:93]
	v_mfma_f32_16x16x32_f16 v[86:89], v[210:213], v[234:237], v[86:89]
	v_mfma_f32_16x16x32_f16 v[82:85], v[210:213], v[242:245], v[82:85]
	v_mfma_f32_16x16x32_f16 v[78:81], v[218:221], v[234:237], v[78:81]
	v_mfma_f32_16x16x32_f16 v[74:77], v[218:221], v[242:245], v[74:77]
	v_mfma_f32_16x16x32_f16 v[70:73], v[226:229], v[234:237], v[70:73]
	v_mfma_f32_16x16x32_f16 v[66:69], v[226:229], v[242:245], v[66:69]
	v_readfirstlane_b32 s47, v161
	v_lshl_add_u64 v[246:247], v[246:247], 0, s[36:37]
	s_mov_b32 m0, s47
	v_readfirstlane_b32 s47, v166
	s_barrier
	ds_read_b128 v[198:201], v176 offset:49152
	ds_read_b128 v[202:205], v176 offset:50176
	ds_read_b128 v[206:209], v176 offset:51200
	ds_read_b128 v[210:213], v176 offset:52224
	ds_read_b128 v[214:217], v176 offset:53248
	ds_read_b128 v[218:221], v176 offset:54272
	ds_read_b128 v[222:225], v176 offset:55296
	ds_read_b128 v[226:229], v176 offset:56320
	global_load_lds_dwordx4 v[246:247], off
	v_lshl_add_u64 v[246:247], v[248:249], 0, s[36:37]
	s_mov_b32 m0, s47
	s_nop 0
	global_load_lds_dwordx4 v[246:247], off
	s_barrier
	s_waitcnt lgkmcnt(0)
	s_waitcnt lgkmcnt(0)
	v_mfma_f32_16x16x32_f16 v[62:65], v[198:201], v[182:185], v[62:65]
	v_mfma_f32_16x16x32_f16 v[58:61], v[198:201], v[190:193], v[58:61]
	v_mfma_f32_16x16x32_f16 v[54:57], v[206:209], v[182:185], v[54:57]
	v_mfma_f32_16x16x32_f16 v[50:53], v[206:209], v[190:193], v[50:53]
	v_mfma_f32_16x16x32_f16 v[46:49], v[214:217], v[182:185], v[46:49]
	v_mfma_f32_16x16x32_f16 v[42:45], v[214:217], v[190:193], v[42:45]
	v_mfma_f32_16x16x32_f16 v[38:41], v[222:225], v[182:185], v[38:41]
	v_mfma_f32_16x16x32_f16 v[34:37], v[222:225], v[190:193], v[34:37]
	v_mfma_f32_16x16x32_f16 v[62:65], v[202:205], v[186:189], v[62:65]
	v_mfma_f32_16x16x32_f16 v[58:61], v[202:205], v[194:197], v[58:61]
	v_mfma_f32_16x16x32_f16 v[54:57], v[210:213], v[186:189], v[54:57]
	v_mfma_f32_16x16x32_f16 v[50:53], v[210:213], v[194:197], v[50:53]
	v_mfma_f32_16x16x32_f16 v[46:49], v[218:221], v[186:189], v[46:49]
	v_mfma_f32_16x16x32_f16 v[42:45], v[218:221], v[194:197], v[42:45]
	v_mfma_f32_16x16x32_f16 v[38:41], v[226:229], v[186:189], v[38:41]
	v_mfma_f32_16x16x32_f16 v[34:37], v[226:229], v[194:197], v[34:37]
	s_barrier
	v_readfirstlane_b32 s47, v168
	v_lshl_add_u64 v[182:183], v[250:251], 0, s[38:39]
	s_mov_b32 m0, s47
	v_readfirstlane_b32 s47, v169
	global_load_lds_dwordx4 v[182:183], off
	v_lshl_add_u64 v[182:183], v[252:253], 0, s[38:39]
	s_mov_b32 m0, s47
	s_nop 0
	global_load_lds_dwordx4 v[182:183], off
	s_waitcnt vmcnt(6)
	s_barrier
	v_mfma_f32_16x16x32_f16 v[30:33], v[198:201], v[230:233], v[30:33]
	v_mfma_f32_16x16x32_f16 v[26:29], v[198:201], v[238:241], v[26:29]
	v_mfma_f32_16x16x32_f16 v[22:25], v[206:209], v[230:233], v[22:25]
	v_mfma_f32_16x16x32_f16 v[18:21], v[206:209], v[238:241], v[18:21]
	v_mfma_f32_16x16x32_f16 v[14:17], v[214:217], v[230:233], v[14:17]
	v_mfma_f32_16x16x32_f16 v[10:13], v[214:217], v[238:241], v[10:13]
	v_mfma_f32_16x16x32_f16 v[6:9], v[222:225], v[230:233], v[6:9]
	v_mfma_f32_16x16x32_f16 v[2:5], v[222:225], v[238:241], v[2:5]
	v_mfma_f32_16x16x32_f16 v[30:33], v[202:205], v[234:237], v[30:33]
	v_mfma_f32_16x16x32_f16 v[26:29], v[202:205], v[242:245], v[26:29]
	v_mfma_f32_16x16x32_f16 v[22:25], v[210:213], v[234:237], v[22:25]
	v_mfma_f32_16x16x32_f16 v[18:21], v[210:213], v[242:245], v[18:21]
	v_mfma_f32_16x16x32_f16 v[14:17], v[218:221], v[234:237], v[14:17]
	v_mfma_f32_16x16x32_f16 v[10:13], v[218:221], v[242:245], v[10:13]
	v_mfma_f32_16x16x32_f16 v[6:9], v[226:229], v[234:237], v[6:9]
	v_mfma_f32_16x16x32_f16 v[2:5], v[226:229], v[242:245], v[2:5]
	s_add_i32 s46, s46, 2
	s_add_u32 s44, s44, 0x100
	s_addc_u32 s45, s45, 0
	s_cmp_lt_u32 s46, 28
	s_barrier
	s_cbranch_scc1 .LBB10_12
	s_add_u32 s42, s42, 0x80f80
	s_addc_u32 s43, s43, 0
	v_readfirstlane_b32 s44, v177
	v_lshl_add_u64 v[130:131], v[130:131], 1, s[42:43]
	s_mov_b32 m0, s44
	ds_read_b128 v[134:137], v171
	ds_read_b128 v[138:141], v173
	ds_read_b128 v[154:157], v174
	ds_read_b128 v[168:171], v175
	ds_read_b128 v[182:185], v176
	ds_read_b128 v[186:189], v176 offset:1024
	ds_read_b128 v[190:193], v176 offset:2048
	ds_read_b128 v[194:197], v176 offset:3072
	ds_read_b128 v[198:201], v176 offset:4096
	ds_read_b128 v[202:205], v176 offset:5120
	ds_read_b128 v[206:209], v176 offset:6144
	ds_read_b128 v[210:213], v176 offset:7168
	global_load_lds_dwordx4 v[130:131], off
	v_lshl_add_u64 v[130:131], v[132:133], 1, s[42:43]
	v_readfirstlane_b32 s42, v178
	s_mov_b32 m0, s42
	s_nop 0
	global_load_lds_dwordx4 v[130:131], off
	s_barrier
	s_waitcnt lgkmcnt(0)
	s_waitcnt lgkmcnt(0)
	v_mfma_f32_16x16x32_f16 v[122:125], v[182:185], v[154:157], v[122:125]
	v_mfma_f32_16x16x32_f16 v[110:113], v[198:201], v[134:137], v[110:113]
	v_mfma_f32_16x16x32_f16 v[98:101], v[206:209], v[154:157], v[98:101]
	v_mfma_f32_16x16x32_f16 v[126:129], v[182:185], v[134:137], v[126:129]
	v_mfma_f32_16x16x32_f16 v[122:125], v[186:189], v[168:171], v[122:125]
	v_mfma_f32_16x16x32_f16 v[118:121], v[190:193], v[134:137], v[118:121]
	v_mfma_f32_16x16x32_f16 v[114:117], v[190:193], v[154:157], v[114:117]
	v_mfma_f32_16x16x32_f16 v[130:133], v[202:205], v[138:141], v[110:113]
	v_mfma_f32_16x16x32_f16 v[106:109], v[198:201], v[154:157], v[106:109]
	v_mfma_f32_16x16x32_f16 v[102:105], v[206:209], v[134:137], v[102:105]
	v_mfma_f32_16x16x32_f16 v[98:101], v[210:213], v[168:171], v[98:101]
	v_mfma_f32_16x16x32_f16 v[126:129], v[186:189], v[138:141], v[126:129]
	v_mfma_f32_16x16x32_f16 v[118:121], v[194:197], v[138:141], v[118:121]
	v_mfma_f32_16x16x32_f16 v[114:117], v[194:197], v[168:171], v[114:117]
	v_mfma_f32_16x16x32_f16 v[214:217], v[202:205], v[168:171], v[106:109]
	v_mfma_f32_16x16x32_f16 v[102:105], v[210:213], v[138:141], v[102:105]
	s_barrier
	ds_read_b128 v[106:109], v162
	ds_read_b128 v[110:113], v163
	ds_read_b128 v[160:163], v164
	ds_read_b128 v[218:221], v165
	s_barrier
	s_waitcnt lgkmcnt(0)
	s_waitcnt lgkmcnt(0)
	v_mfma_f32_16x16x32_f16 v[82:85], v[190:193], v[160:163], v[82:85]
	v_mfma_f32_16x16x32_f16 v[78:81], v[198:201], v[106:109], v[78:81]
	v_mfma_f32_16x16x32_f16 v[74:77], v[198:201], v[160:163], v[74:77]
	v_mfma_f32_16x16x32_f16 v[70:73], v[206:209], v[106:109], v[70:73]
	v_mfma_f32_16x16x32_f16 v[66:69], v[206:209], v[160:163], v[66:69]
	v_mfma_f32_16x16x32_f16 v[94:97], v[182:185], v[106:109], v[94:97]
	v_mfma_f32_16x16x32_f16 v[90:93], v[182:185], v[160:163], v[90:93]
	v_mfma_f32_16x16x32_f16 v[86:89], v[190:193], v[106:109], v[86:89]
	v_mfma_f32_16x16x32_f16 v[82:85], v[194:197], v[218:221], v[82:85]
	v_mfma_f32_16x16x32_f16 v[78:81], v[202:205], v[110:113], v[78:81]
	v_mfma_f32_16x16x32_f16 v[74:77], v[202:205], v[218:221], v[74:77]
	v_mfma_f32_16x16x32_f16 v[70:73], v[210:213], v[110:113], v[70:73]
	v_mfma_f32_16x16x32_f16 v[66:69], v[210:213], v[218:221], v[66:69]
	v_mfma_f32_16x16x32_f16 v[222:225], v[186:189], v[110:113], v[94:97]
	v_mfma_f32_16x16x32_f16 v[182:185], v[186:189], v[218:221], v[90:93]
	v_mfma_f32_16x16x32_f16 v[86:89], v[194:197], v[110:113], v[86:89]
	s_barrier
	ds_read_b128 v[90:93], v176 offset:16384
	ds_read_b128 v[94:97], v176 offset:17408
	ds_read_b128 v[186:189], v176 offset:18432
	ds_read_b128 v[190:193], v176 offset:19456
	ds_read_b128 v[194:197], v176 offset:20480
	ds_read_b128 v[198:201], v176 offset:21504
	ds_read_b128 v[202:205], v176 offset:22528
	ds_read_b128 v[206:209], v176 offset:23552
	s_waitcnt vmcnt(4)
	s_barrier
	s_waitcnt lgkmcnt(0)
	s_waitcnt lgkmcnt(0)
	v_mfma_f32_16x16x32_f16 v[46:49], v[194:197], v[134:137], v[46:49]
	v_mfma_f32_16x16x32_f16 v[42:45], v[194:197], v[154:157], v[42:45]
	v_mfma_f32_16x16x32_f16 v[38:41], v[202:205], v[134:137], v[38:41]
	v_mfma_f32_16x16x32_f16 v[34:37], v[202:205], v[154:157], v[34:37]
	v_mfma_f32_16x16x32_f16 v[62:65], v[90:93], v[134:137], v[62:65]
	v_mfma_f32_16x16x32_f16 v[58:61], v[90:93], v[154:157], v[58:61]
	v_mfma_f32_16x16x32_f16 v[54:57], v[186:189], v[134:137], v[54:57]
	v_mfma_f32_16x16x32_f16 v[50:53], v[186:189], v[154:157], v[50:53]
	v_mfma_f32_16x16x32_f16 v[46:49], v[198:201], v[138:141], v[46:49]
	v_mfma_f32_16x16x32_f16 v[42:45], v[198:201], v[168:171], v[42:45]
	v_mfma_f32_16x16x32_f16 v[38:41], v[206:209], v[138:141], v[38:41]
	v_mfma_f32_16x16x32_f16 v[34:37], v[206:209], v[168:171], v[34:37]
	v_mfma_f32_16x16x32_f16 v[210:213], v[94:97], v[138:141], v[62:65]
	v_mfma_f32_16x16x32_f16 v[226:229], v[94:97], v[168:171], v[58:61]
	v_mfma_f32_16x16x32_f16 v[230:233], v[190:193], v[138:141], v[54:57]
	v_mfma_f32_16x16x32_f16 v[234:237], v[190:193], v[168:171], v[50:53]
	v_mfma_f32_16x16x32_f16 v[2:5], v[202:205], v[160:163], v[2:5]
	v_mfma_f32_16x16x32_f16 v[30:33], v[90:93], v[106:109], v[30:33]
	v_mfma_f32_16x16x32_f16 v[26:29], v[90:93], v[160:163], v[26:29]
	v_mfma_f32_16x16x32_f16 v[22:25], v[186:189], v[106:109], v[22:25]
	v_mfma_f32_16x16x32_f16 v[18:21], v[186:189], v[160:163], v[18:21]
	v_mfma_f32_16x16x32_f16 v[14:17], v[194:197], v[106:109], v[14:17]
	v_mfma_f32_16x16x32_f16 v[10:13], v[194:197], v[160:163], v[10:13]
	v_mfma_f32_16x16x32_f16 v[6:9], v[202:205], v[106:109], v[6:9]
	v_mfma_f32_16x16x32_f16 v[2:5], v[206:209], v[218:221], v[2:5]
	v_mfma_f32_16x16x32_f16 v[138:141], v[94:97], v[110:113], v[30:33]
	v_mfma_f32_16x16x32_f16 v[168:171], v[94:97], v[218:221], v[26:29]
	v_mfma_f32_16x16x32_f16 v[238:241], v[190:193], v[110:113], v[22:25]
	v_mfma_f32_16x16x32_f16 v[186:189], v[190:193], v[218:221], v[18:21]
	v_mfma_f32_16x16x32_f16 v[190:193], v[198:201], v[110:113], v[14:17]
	v_mfma_f32_16x16x32_f16 v[194:197], v[198:201], v[218:221], v[10:13]
	v_mfma_f32_16x16x32_f16 v[198:201], v[206:209], v[110:113], v[6:9]
	s_barrier
	s_nop 0
	ds_read_b128 v[6:9], v144
	ds_read_b128 v[10:13], v145
	ds_read_b128 v[14:17], v146
	ds_read_b128 v[160:163], v147
	ds_read_b128 v[18:21], v176 offset:32768
	ds_read_b128 v[22:25], v176 offset:33792
	ds_read_b128 v[26:29], v176 offset:34816
	ds_read_b128 v[50:53], v176 offset:35840
	ds_read_b128 v[202:205], v176 offset:36864
	ds_read_b128 v[206:209], v176 offset:37888
	ds_read_b128 v[218:221], v176 offset:38912
	ds_read_b128 v[242:245], v176 offset:39936
	s_waitcnt vmcnt(2)
	s_barrier
	s_waitcnt lgkmcnt(0)
	s_waitcnt lgkmcnt(0)
	v_mfma_f32_16x16x32_f16 v[30:33], v[18:21], v[6:9], v[126:129]
	v_mfma_f32_16x16x32_f16 v[154:157], v[22:25], v[10:13], v[30:33]
	v_mfma_f32_16x16x32_f16 v[30:33], v[18:21], v[14:17], v[122:125]
	v_mfma_f32_16x16x32_f16 v[110:113], v[22:25], v[160:163], v[30:33]
	v_mfma_f32_16x16x32_f16 v[30:33], v[26:29], v[6:9], v[118:121]
	v_mfma_f32_16x16x32_f16 v[146:149], v[50:53], v[10:13], v[30:33]
	v_mfma_f32_16x16x32_f16 v[30:33], v[26:29], v[14:17], v[114:117]
	v_mfma_f32_16x16x32_f16 v[106:109], v[50:53], v[160:163], v[30:33]
	v_mfma_f32_16x16x32_f16 v[30:33], v[202:205], v[6:9], v[130:133]
	v_mfma_f32_16x16x32_f16 v[142:145], v[206:209], v[10:13], v[30:33]
	v_mfma_f32_16x16x32_f16 v[30:33], v[202:205], v[14:17], v[214:217]
	v_mfma_f32_16x16x32_f16 v[94:97], v[206:209], v[160:163], v[30:33]
	v_mfma_f32_16x16x32_f16 v[30:33], v[218:221], v[6:9], v[102:105]
	v_mfma_f32_16x16x32_f16 v[134:137], v[242:245], v[10:13], v[30:33]
	v_mfma_f32_16x16x32_f16 v[30:33], v[218:221], v[14:17], v[98:101]
	v_mfma_f32_16x16x32_f16 v[90:93], v[242:245], v[160:163], v[30:33]
	s_barrier
	ds_read_b128 v[102:105], v150
	ds_read_b128 v[114:117], v151
	ds_read_b128 v[118:121], v152
	ds_read_b128 v[126:129], v153
	s_waitcnt vmcnt(0)
	s_barrier
	s_waitcnt lgkmcnt(0)
	s_waitcnt lgkmcnt(0)
	v_mfma_f32_16x16x32_f16 v[30:33], v[18:21], v[102:105], v[222:225]
	v_mfma_f32_16x16x32_f16 v[18:21], v[18:21], v[118:121], v[182:185]
	v_mfma_f32_16x16x32_f16 v[62:65], v[22:25], v[114:117], v[30:33]
	v_mfma_f32_16x16x32_f16 v[30:33], v[22:25], v[126:129], v[18:21]
	v_mfma_f32_16x16x32_f16 v[18:21], v[26:29], v[102:105], v[86:89]
	v_mfma_f32_16x16x32_f16 v[58:61], v[50:53], v[114:117], v[18:21]
	v_mfma_f32_16x16x32_f16 v[18:21], v[26:29], v[118:121], v[82:85]
	v_mfma_f32_16x16x32_f16 v[26:29], v[50:53], v[126:129], v[18:21]
	v_mfma_f32_16x16x32_f16 v[18:21], v[202:205], v[102:105], v[78:81]
	v_mfma_f32_16x16x32_f16 v[54:57], v[206:209], v[114:117], v[18:21]
	v_mfma_f32_16x16x32_f16 v[18:21], v[202:205], v[118:121], v[74:77]
	v_mfma_f32_16x16x32_f16 v[22:25], v[206:209], v[126:129], v[18:21]
	v_mfma_f32_16x16x32_f16 v[18:21], v[218:221], v[102:105], v[70:73]
	v_mfma_f32_16x16x32_f16 v[50:53], v[242:245], v[114:117], v[18:21]
	v_mfma_f32_16x16x32_f16 v[18:21], v[218:221], v[118:121], v[66:69]
	v_mfma_f32_16x16x32_f16 v[18:21], v[242:245], v[126:129], v[18:21]
	s_barrier
	ds_read_b128 v[86:89], v176 offset:49152
	ds_read_b128 v[150:153], v176 offset:50176
	ds_read_b128 v[182:185], v176 offset:51200
	ds_read_b128 v[202:205], v176 offset:52224
	ds_read_b128 v[206:209], v176 offset:53248
	ds_read_b128 v[214:217], v176 offset:54272
	ds_read_b128 v[218:221], v176 offset:55296
	ds_read_b128 v[174:177], v176 offset:56320
	s_barrier
	s_waitcnt lgkmcnt(0)
	s_waitcnt lgkmcnt(0)
	v_mfma_f32_16x16x32_f16 v[66:69], v[86:89], v[6:9], v[210:213]
	v_mfma_f32_16x16x32_f16 v[130:133], v[150:153], v[10:13], v[66:69]
	v_mfma_f32_16x16x32_f16 v[66:69], v[86:89], v[14:17], v[226:229]
	v_mfma_f32_16x16x32_f16 v[78:81], v[150:153], v[160:163], v[66:69]
	v_mfma_f32_16x16x32_f16 v[66:69], v[182:185], v[6:9], v[230:233]
	v_mfma_f32_16x16x32_f16 v[46:49], v[206:209], v[6:9], v[46:49]
	v_mfma_f32_16x16x32_f16 v[6:9], v[218:221], v[6:9], v[38:41]
	v_mfma_f32_16x16x32_f16 v[122:125], v[202:205], v[10:13], v[66:69]
	v_mfma_f32_16x16x32_f16 v[66:69], v[182:185], v[14:17], v[234:237]
	v_mfma_f32_16x16x32_f16 v[42:45], v[206:209], v[14:17], v[42:45]
	v_mfma_f32_16x16x32_f16 v[82:85], v[174:177], v[10:13], v[6:9]
	v_mfma_f32_16x16x32_f16 v[6:9], v[218:221], v[14:17], v[34:37]
	v_mfma_f32_16x16x32_f16 v[74:77], v[202:205], v[160:163], v[66:69]
	v_mfma_f32_16x16x32_f16 v[98:101], v[214:217], v[10:13], v[46:49]
	v_mfma_f32_16x16x32_f16 v[70:73], v[214:217], v[160:163], v[42:45]
	v_mfma_f32_16x16x32_f16 v[66:69], v[174:177], v[160:163], v[6:9]
	v_mfma_f32_16x16x32_f16 v[6:9], v[86:89], v[102:105], v[138:141]
	v_mfma_f32_16x16x32_f16 v[46:49], v[150:153], v[114:117], v[6:9]
	v_mfma_f32_16x16x32_f16 v[6:9], v[86:89], v[118:121], v[168:171]
	v_mfma_f32_16x16x32_f16 v[14:17], v[150:153], v[126:129], v[6:9]
	v_mfma_f32_16x16x32_f16 v[6:9], v[182:185], v[102:105], v[238:241]
	v_mfma_f32_16x16x32_f16 v[42:45], v[202:205], v[114:117], v[6:9]
	v_mfma_f32_16x16x32_f16 v[6:9], v[182:185], v[118:121], v[186:189]
	v_mfma_f32_16x16x32_f16 v[10:13], v[202:205], v[126:129], v[6:9]
	v_mfma_f32_16x16x32_f16 v[6:9], v[206:209], v[102:105], v[190:193]
	v_mfma_f32_16x16x32_f16 v[38:41], v[214:217], v[114:117], v[6:9]
	v_mfma_f32_16x16x32_f16 v[6:9], v[206:209], v[118:121], v[194:197]
	v_mfma_f32_16x16x32_f16 v[34:37], v[218:221], v[102:105], v[198:201]
	v_mfma_f32_16x16x32_f16 v[2:5], v[218:221], v[118:121], v[2:5]
	v_mfma_f32_16x16x32_f16 v[6:9], v[214:217], v[126:129], v[6:9]
	v_mfma_f32_16x16x32_f16 v[34:37], v[174:177], v[114:117], v[34:37]
	v_mfma_f32_16x16x32_f16 v[2:5], v[174:177], v[126:129], v[2:5]
	s_cmpk_gt_u32 s61, 0xff
	s_barrier
	s_cbranch_scc1 .LBB10_15
	s_barrier
